# epilogue stores widened to full-row dwordx4 via LDS transpose in L1,L2,L3 GEMM kernels; prologue drain waits removed
# speedup vs baseline: 1.0489x; 1.0489x over previous
_Z16gemm_glds_kernelILi2EEvPKDF16_PDF16_PKiS4_S1_S1_PKfiS6_Pc:
	s_load_dword s3, s[0:1], 0x38
	s_mov_b64 s[4:5], -1
	s_waitcnt lgkmcnt(0)
	s_cmp_lt_i32 s2, s3
	s_cbranch_scc1 .LBB2_2
	s_load_dwordx4 s[4:7], s[0:1], 0x40
	s_sub_i32 s3, s2, s3
	v_lshrrev_b32_e32 v1, 8, v0
	s_lshl_b32 s8, s3, 1
	v_or_b32_e32 v6, s8, v1
	s_bfe_u32 s8, s3, 0x180007
	v_mov_b32_e32 v4, 0x3d2844
	s_waitcnt lgkmcnt(0)
	v_mov_b64_e32 v[2:3], s[4:5]
	v_mad_u64_u32 v[4:5], s[4:5], s8, v4, v[2:3]
	v_lshlrev_b32_e32 v2, 6, v6
	v_and_b32_e32 v26, 0x3c0, v2
	v_and_b32_e32 v22, 63, v0
	s_lshl_b32 s3, s3, 3
	v_or_b32_e32 v23, v26, v22
	s_and_b32 s3, s3, 0x3c0
	v_bfe_u32 v24, v0, 6, 2
	v_min_u32_e32 v2, 0x3e8, v23
	v_lshlrev_b32_e32 v2, 2, v2
	v_mov_b32_e32 v3, 0
	v_or_b32_e32 v25, s3, v24
	v_lshl_add_u64 v[4:5], v[4:5], 0, v[2:3]
	v_mul_u32_u24_e32 v2, 0xfa4, v25
	v_lshl_add_u64 v[6:7], v[4:5], 0, v[2:3]
	v_or_b32_e32 v2, 4, v25
	v_mul_u32_u24_e32 v2, 0xfa4, v2
	v_lshl_add_u64 v[8:9], v[4:5], 0, v[2:3]
	v_or_b32_e32 v2, 8, v25
	v_mul_u32_u24_e32 v2, 0xfa4, v2
	v_lshl_add_u64 v[10:11], v[4:5], 0, v[2:3]
	v_or_b32_e32 v2, 12, v25
	v_mul_u32_u24_e32 v2, 0xfa4, v2
	v_lshl_add_u64 v[12:13], v[4:5], 0, v[2:3]
	v_or_b32_e32 v2, 16, v25
	v_mul_u32_u24_e32 v2, 0xfa4, v2
	v_lshl_add_u64 v[14:15], v[4:5], 0, v[2:3]
	v_or_b32_e32 v2, 20, v25
	v_mul_u32_u24_e32 v2, 0xfa4, v2
	v_lshl_add_u64 v[16:17], v[4:5], 0, v[2:3]
	v_or_b32_e32 v2, 24, v25
	v_mul_u32_u24_e32 v2, 0xfa4, v2
	v_lshl_add_u64 v[18:19], v[4:5], 0, v[2:3]
	v_or_b32_e32 v2, 28, v25
	v_mul_u32_u24_e32 v2, 0xfa4, v2
	v_lshl_add_u64 v[20:21], v[4:5], 0, v[2:3]
	v_or_b32_e32 v2, 32, v25
	v_mul_u32_u24_e32 v2, 0xfa4, v2
	global_load_dword v27, v[6:7], off
	global_load_dword v28, v[8:9], off
	global_load_dword v29, v[10:11], off
	global_load_dword v30, v[12:13], off
	global_load_dword v31, v[14:15], off
	global_load_dword v32, v[16:17], off
	global_load_dword v33, v[18:19], off
	global_load_dword v34, v[20:21], off
	v_lshl_add_u64 v[6:7], v[4:5], 0, v[2:3]
	v_or_b32_e32 v2, 36, v25
	v_mul_u32_u24_e32 v2, 0xfa4, v2
	v_or_b32_e32 v12, 40, v25
	v_lshl_add_u64 v[8:9], v[4:5], 0, v[2:3]
	v_min_u32_e32 v2, 0x3e8, v12
	v_mul_u32_u24_e32 v2, 0xfa4, v2
	v_lshl_add_u64 v[10:11], v[4:5], 0, v[2:3]
	global_load_dword v13, v[6:7], off
	global_load_dword v14, v[8:9], off
	global_load_dword v15, v[10:11], off
	v_or_b32_e32 v10, 44, v25
	v_min_u32_e32 v2, 0x3e8, v10
	v_mul_u32_u24_e32 v2, 0xfa4, v2
	v_or_b32_e32 v11, 48, v25
	v_lshl_add_u64 v[6:7], v[4:5], 0, v[2:3]
	v_min_u32_e32 v2, 0x3e8, v11
	v_mul_u32_u24_e32 v2, 0xfa4, v2
	v_lshl_add_u64 v[8:9], v[4:5], 0, v[2:3]
	global_load_dword v16, v[6:7], off
	global_load_dword v17, v[8:9], off
	v_or_b32_e32 v8, 52, v25
	v_min_u32_e32 v2, 0x3e8, v8
	v_mul_u32_u24_e32 v2, 0xfa4, v2
	v_or_b32_e32 v18, 56, v25
	v_lshl_add_u64 v[6:7], v[4:5], 0, v[2:3]
	v_min_u32_e32 v2, 0x3e8, v18
	v_mul_u32_u24_e32 v2, 0xfa4, v2
	global_load_dword v9, v[6:7], off
	v_lshl_add_u64 v[6:7], v[4:5], 0, v[2:3]
	global_load_dword v6, v[6:7], off
	v_or_b32_e32 v7, 60, v25
	v_min_u32_e32 v2, 0x3e8, v7
	v_mul_u32_u24_e32 v2, 0xfa4, v2
	v_lshl_add_u64 v[4:5], v[4:5], 0, v[2:3]
	global_load_dword v2, v[4:5], off
	s_movk_i32 s4, 0x4100
	s_movk_i32 s10, 0x3e9
	v_mad_u32_u24 v1, v1, s4, 0
	v_lshlrev_b32_e32 v4, 2, v22
	v_cmp_gt_u32_e32 vcc, s10, v23
	v_mul_u32_u24_e32 v19, 0x104, v24
	v_add3_u32 v4, v1, v4, v19
	v_cmp_gt_u32_e64 s[4:5], s10, v12
	s_and_b64 s[4:5], s[4:5], vcc
	s_mov_b32 s9, 0
	s_lshl_b64 s[8:9], s[8:9], 21
	s_waitcnt vmcnt(15)
	v_cndmask_b32_e32 v5, 0, v27, vcc
	ds_write_b32 v4, v5
	s_waitcnt vmcnt(14)
	v_cndmask_b32_e32 v5, 0, v28, vcc
	ds_write_b32 v4, v5 offset:1040
	s_waitcnt vmcnt(13)
	v_cndmask_b32_e32 v5, 0, v29, vcc
	ds_write_b32 v4, v5 offset:2080
	s_waitcnt vmcnt(12)
	v_cndmask_b32_e32 v5, 0, v30, vcc
	ds_write_b32 v4, v5 offset:3120
	s_waitcnt vmcnt(11)
	v_cndmask_b32_e32 v5, 0, v31, vcc
	ds_write_b32 v4, v5 offset:4160
	s_waitcnt vmcnt(10)
	v_cndmask_b32_e32 v5, 0, v32, vcc
	ds_write_b32 v4, v5 offset:5200
	s_waitcnt vmcnt(9)
	v_cndmask_b32_e32 v5, 0, v33, vcc
	ds_write_b32 v4, v5 offset:6240
	s_waitcnt vmcnt(8)
	v_cndmask_b32_e32 v5, 0, v34, vcc
	ds_write_b32 v4, v5 offset:7280
	s_waitcnt vmcnt(7)
	v_cndmask_b32_e32 v5, 0, v13, vcc
	ds_write_b32 v4, v5 offset:8320
	s_waitcnt vmcnt(6)
	v_cndmask_b32_e32 v5, 0, v14, vcc
	ds_write_b32 v4, v5 offset:9360
	s_waitcnt vmcnt(5)
	v_cndmask_b32_e64 v5, 0, v15, s[4:5]
	v_cmp_gt_u32_e64 s[4:5], s10, v10
	s_and_b64 s[4:5], s[4:5], vcc
	ds_write_b32 v4, v5 offset:10400
	s_waitcnt vmcnt(4)
	v_cndmask_b32_e64 v5, 0, v16, s[4:5]
	v_cmp_gt_u32_e64 s[4:5], s10, v11
	s_and_b64 s[4:5], s[4:5], vcc
	ds_write_b32 v4, v5 offset:11440
	s_waitcnt vmcnt(3)
	v_cndmask_b32_e64 v5, 0, v17, s[4:5]
	v_cmp_gt_u32_e64 s[4:5], s10, v8
	s_and_b64 s[4:5], s[4:5], vcc
	ds_write_b32 v4, v5 offset:12480
	s_waitcnt vmcnt(2)
	v_cndmask_b32_e64 v5, 0, v9, s[4:5]
	v_cmp_gt_u32_e64 s[4:5], s10, v18
	s_and_b64 s[4:5], s[4:5], vcc
	ds_write_b32 v4, v5 offset:13520
	s_waitcnt vmcnt(1)
	v_cndmask_b32_e64 v5, 0, v6, s[4:5]
	v_cmp_gt_u32_e64 s[4:5], s10, v7
	s_and_b64 vcc, s[4:5], vcc
	s_waitcnt vmcnt(0)
	v_cndmask_b32_e32 v2, 0, v2, vcc
	s_add_u32 s4, s6, s8
	ds_write_b32 v4, v2 offset:15600
	s_addc_u32 s5, s7, s9
	v_lshlrev_b32_e32 v2, 3, v0
	s_lshl_b32 s3, s3, 1
	v_and_b32_e32 v6, 56, v2
	s_add_u32 s4, s4, s3
	s_addc_u32 s5, s5, 0
	v_lshlrev_b32_e32 v2, 1, v6
	ds_write_b32 v4, v5 offset:14560
	v_lshl_add_u64 v[4:5], s[4:5], 0, v[2:3]
	v_bfe_u32 v2, v0, 3, 5
	v_lshlrev_b32_e32 v7, 2, v2
	v_mul_u32_u24_e32 v6, 0x104, v6
	v_add3_u32 v1, v1, v7, v6
	v_add_u32_e32 v6, 0x400, v1
	s_waitcnt lgkmcnt(0)
	s_barrier
	ds_read2_b32 v[8:9], v1 offset1:32
	ds_read2_b32 v[10:11], v1 offset0:130 offset1:162
	ds_read2_b32 v[12:13], v6 offset0:4 offset1:36
	ds_read2_b32 v[14:15], v6 offset0:134 offset1:166
	ds_read2_b32 v[16:17], v6 offset0:199 offset1:231
	ds_read2_b32 v[18:19], v6 offset0:69 offset1:101
	ds_read2_b32 v[20:21], v1 offset0:195 offset1:227
	ds_read2_b32 v[22:23], v1 offset0:65 offset1:97
	s_mov_b64 s[4:5], 0x800000
	v_or_b32_e32 v1, v26, v2
	v_lshl_add_u64 v[24:25], v[4:5], 0, s[4:5]
	v_lshlrev_b32_e32 v2, 11, v1
	s_waitcnt lgkmcnt(3)
	v_cvt_pk_f16_f32 v7, v14, v16
	s_waitcnt lgkmcnt(2)
	v_cvt_pk_f16_f32 v6, v12, v18
	s_waitcnt lgkmcnt(1)
	v_cvt_pk_f16_f32 v5, v10, v20
	s_waitcnt lgkmcnt(0)
	v_cvt_pk_f16_f32 v4, v8, v22
	v_lshl_add_u64 v[26:27], v[24:25], 0, v[2:3]
	v_or_b32_e32 v2, 0x10000, v2
	global_store_dwordx4 v[26:27], v[4:7], off
	v_lshl_add_u64 v[2:3], v[24:25], 0, v[2:3]
	s_mov_b64 s[4:5], 0
	v_cvt_pk_f16_f32 v7, v15, v17
	v_cvt_pk_f16_f32 v6, v13, v19
	v_cvt_pk_f16_f32 v5, v11, v21
	v_cvt_pk_f16_f32 v4, v9, v23
	global_store_dwordx4 v[2:3], v[4:7], off

.LBB2_5:
	s_mul_i32 s4, s14, 0xc000
	s_add_i32 s5, s4, 0
	s_add_i32 s16, s5, s11
	s_add_i32 s5, s5, s13
	v_add_u32_e32 v134, s5, v89
	s_waitcnt vmcnt(6)
	s_barrier
	v_add_u32_e32 v118, v134, v87
	ds_read_b128 v[102:105], v118 offset:16384
	ds_read_b128 v[110:113], v118 offset:18432
	v_add_u32_e32 v130, s16, v89
	v_add_u32_e32 v126, v130, v87
	ds_read_b128 v[106:109], v126
	s_waitcnt lgkmcnt(0)
	v_mfma_f32_16x16x32_f16 v[18:21], v[102:105], v[106:109], v[18:21]
	ds_read_b128 v[114:117], v118 offset:20480
	v_add_u32_e32 v150, v130, v85
	v_add_u32_e32 v142, v134, v85
	v_mfma_f32_16x16x32_f16 v[22:25], v[110:113], v[106:109], v[22:25]
	ds_read_b128 v[118:121], v118 offset:22528
	s_add_i32 s4, s4, 0xffff4000
	s_cmp_lg_u32 s14, 0
	s_waitcnt lgkmcnt(0)
	v_mfma_f32_16x16x32_f16 v[26:29], v[114:117], v[106:109], v[26:29]
	ds_read_b128 v[122:125], v126 offset:2048
	s_cselect_b32 s4, s4, 0x18000
	s_add_i32 s4, s4, 0
	v_mfma_f32_16x16x32_f16 v[30:33], v[118:121], v[106:109], v[30:33]
	ds_read_b128 v[106:109], v126 offset:4096
	s_add_i32 s5, s4, s9
	s_mov_b32 m0, s5
	s_waitcnt lgkmcnt(0)
	v_mfma_f32_16x16x32_f16 v[38:41], v[102:105], v[122:125], v[38:41]
	ds_read_b128 v[126:129], v126 offset:6144
	s_add_i32 s4, s4, s12
	v_mfma_f32_16x16x32_f16 v[42:45], v[110:113], v[122:125], v[42:45]
	ds_read_b128 v[130:133], v150
	v_mfma_f32_16x16x32_f16 v[50:53], v[114:117], v[122:125], v[50:53]
	ds_read_b128 v[134:137], v142 offset:16384
	v_mfma_f32_16x16x32_f16 v[46:49], v[118:121], v[122:125], v[46:49]
	ds_read_b128 v[122:125], v142 offset:18432
	v_mfma_f32_16x16x32_f16 v[54:57], v[102:105], v[106:109], v[54:57]
	ds_read_b128 v[138:141], v142 offset:20480
	v_mfma_f32_16x16x32_f16 v[58:61], v[110:113], v[106:109], v[58:61]
	ds_read_b128 v[142:145], v142 offset:22528
	v_mfma_f32_16x16x32_f16 v[62:65], v[114:117], v[106:109], v[62:65]
	ds_read_b128 v[146:149], v150 offset:2048
	v_mfma_f32_16x16x32_f16 v[66:69], v[118:121], v[106:109], v[66:69]
	ds_read_b128 v[106:109], v150 offset:4096
	s_waitcnt lgkmcnt(0)
	v_mfma_f32_16x16x32_f16 v[70:73], v[102:105], v[126:129], v[70:73]
	ds_read_b128 v[102:105], v150 offset:6144
	v_mfma_f32_16x16x32_f16 v[74:77], v[110:113], v[126:129], v[74:77]
	v_lshl_add_u64 v[110:111], v[100:101], 0, s[2:3]
	v_mfma_f32_16x16x32_f16 v[34:37], v[114:117], v[126:129], v[34:37]
	v_mfma_f32_16x16x32_f16 v[78:81], v[118:121], v[126:129], v[78:81]
	global_load_lds_dwordx4 v[110:111], off
	v_lshl_add_u64 v[110:111], v[98:99], 0, s[2:3]
	s_add_i32 m0, s5, 0x400
	v_mfma_f32_16x16x32_f16 v[18:21], v[134:137], v[130:133], v[18:21]
	v_mfma_f32_16x16x32_f16 v[22:25], v[122:125], v[130:133], v[22:25]
	v_mfma_f32_16x16x32_f16 v[26:29], v[138:141], v[130:133], v[26:29]
	global_load_lds_dwordx4 v[110:111], off
	v_lshl_add_u64 v[110:111], v[96:97], 0, s[2:3]
	s_add_i32 m0, s4, 0x4000
	v_mfma_f32_16x16x32_f16 v[30:33], v[142:145], v[130:133], v[30:33]
	v_mfma_f32_16x16x32_f16 v[38:41], v[134:137], v[146:149], v[38:41]
	v_mfma_f32_16x16x32_f16 v[42:45], v[122:125], v[146:149], v[42:45]
	global_load_lds_dwordx4 v[110:111], off
	v_lshl_add_u64 v[110:111], v[94:95], 0, s[2:3]
	s_add_i32 m0, s4, 0x4400
	v_mfma_f32_16x16x32_f16 v[50:53], v[138:141], v[146:149], v[50:53]
	v_mfma_f32_16x16x32_f16 v[46:49], v[142:145], v[146:149], v[46:49]
	v_mfma_f32_16x16x32_f16 v[54:57], v[134:137], v[106:109], v[54:57]
	global_load_lds_dwordx4 v[110:111], off
	v_lshl_add_u64 v[110:111], v[92:93], 0, s[2:3]
	s_add_i32 m0, s4, 0x4800
	v_mfma_f32_16x16x32_f16 v[58:61], v[122:125], v[106:109], v[58:61]
	v_mfma_f32_16x16x32_f16 v[62:65], v[138:141], v[106:109], v[62:65]
	v_mfma_f32_16x16x32_f16 v[66:69], v[142:145], v[106:109], v[66:69]
	global_load_lds_dwordx4 v[110:111], off
	v_lshl_add_u64 v[106:107], v[90:91], 0, s[2:3]
	s_add_i32 m0, s4, 0x4c00
	s_waitcnt lgkmcnt(0)
	v_mfma_f32_16x16x32_f16 v[70:73], v[134:137], v[102:105], v[70:73]
	s_add_i32 s4, s14, 1
	s_cmp_lg_u32 s14, 2
	s_cselect_b32 s14, s4, 0
	v_mfma_f32_16x16x32_f16 v[74:77], v[122:125], v[102:105], v[74:77]
	s_add_u32 s2, s2, 0x80
	s_addc_u32 s3, s3, 0
	s_cmp_eq_u32 s10, s2
	v_mfma_f32_16x16x32_f16 v[34:37], v[138:141], v[102:105], v[34:37]
	global_load_lds_dwordx4 v[106:107], off
	v_mfma_f32_16x16x32_f16 v[78:81], v[142:145], v[102:105], v[78:81]
	s_cbranch_scc0 .LBB2_5
	s_mul_i32 s3, s14, 0xc000
	v_or_b32_e32 v1, s8, v1
	s_add_i32 s2, s3, 0
	v_lshlrev_b32_e32 v1, 7, v1
	v_add_u32_e32 v122, s2, v1
	s_waitcnt vmcnt(6)
	s_barrier
	v_add_u32_e32 v106, v122, v87
	ds_read_b128 v[90:93], v106 offset:16384
	v_lshlrev_b32_e32 v89, 7, v83
	ds_read_b128 v[98:101], v106 offset:18432
	v_add_u32_e32 v118, s2, v89
	v_add_u32_e32 v114, v118, v87
	ds_read_b128 v[94:97], v114
	s_waitcnt lgkmcnt(0)
	v_mfma_f32_16x16x32_f16 v[18:21], v[90:93], v[94:97], v[18:21]
	ds_read_b128 v[102:105], v106 offset:20480
	v_add_u32_e32 v138, v118, v85
	v_add_u32_e32 v130, v122, v85
	v_mfma_f32_16x16x32_f16 v[22:25], v[98:101], v[94:97], v[22:25]
	ds_read_b128 v[106:109], v106 offset:22528
	s_lshr_b32 s2, s15, 8
	s_add_i32 s3, s3, 0xc000
	s_waitcnt lgkmcnt(0)
	v_mfma_f32_16x16x32_f16 v[26:29], v[102:105], v[94:97], v[26:29]
	ds_read_b128 v[110:113], v114 offset:2048
	s_cmp_lg_u32 s14, 2
	s_cselect_b32 s3, s3, 0
	v_mfma_f32_16x16x32_f16 v[30:33], v[106:109], v[94:97], v[30:33]
	ds_read_b128 v[94:97], v114 offset:4096
	s_add_i32 s3, s3, 0
	v_add_u32_e32 v1, s3, v1
	s_waitcnt lgkmcnt(0)
	v_mfma_f32_16x16x32_f16 v[38:41], v[90:93], v[110:113], v[38:41]
	ds_read_b128 v[114:117], v114 offset:6144
	v_add_u32_e32 v89, s3, v89
	s_lshl_b64 s[0:1], s[0:1], 1
	v_mfma_f32_16x16x32_f16 v[42:45], v[98:101], v[110:113], v[42:45]
	ds_read_b128 v[118:121], v138
	s_add_u32 s0, s6, s0
	s_addc_u32 s1, s7, s1
	v_mfma_f32_16x16x32_f16 v[50:53], v[102:105], v[110:113], v[50:53]
	ds_read_b128 v[122:125], v130 offset:16384
	s_lshl_b32 s3, s8, 1
	s_add_u32 s0, s0, s3
	v_mfma_f32_16x16x32_f16 v[46:49], v[106:109], v[110:113], v[46:49]
	ds_read_b128 v[110:113], v130 offset:18432
	s_addc_u32 s1, s1, 0
	v_lshlrev_b32_e32 v0, 1, v0
	v_mfma_f32_16x16x32_f16 v[54:57], v[90:93], v[94:97], v[54:57]
	ds_read_b128 v[126:129], v130 offset:20480
	v_cmp_gt_u32_e32 vcc, s2, v83
	v_mfma_f32_16x16x32_f16 v[58:61], v[98:101], v[94:97], v[58:61]
	ds_read_b128 v[130:133], v130 offset:22528
	v_mfma_f32_16x16x32_f16 v[62:65], v[102:105], v[94:97], v[62:65]
	ds_read_b128 v[134:137], v138 offset:2048
	v_mfma_f32_16x16x32_f16 v[66:69], v[106:109], v[94:97], v[66:69]
	ds_read_b128 v[94:97], v138 offset:4096
	s_waitcnt lgkmcnt(0)
	v_mfma_f32_16x16x32_f16 v[70:73], v[90:93], v[114:117], v[70:73]
	ds_read_b128 v[90:93], v138 offset:6144
	s_waitcnt vmcnt(0)
	s_barrier
	v_mfma_f32_16x16x32_f16 v[74:77], v[98:101], v[114:117], v[74:77]
	v_mfma_f32_16x16x32_f16 v[34:37], v[102:105], v[114:117], v[34:37]
	v_mfma_f32_16x16x32_f16 v[78:81], v[106:109], v[114:117], v[78:81]
	v_add_u32_e32 v106, v1, v87
	v_add_u32_e32 v87, v89, v87
	v_add_u32_e32 v1, v1, v85
	v_mfma_f32_16x16x32_f16 v[18:21], v[122:125], v[118:121], v[18:21]
	v_mfma_f32_16x16x32_f16 v[22:25], v[110:113], v[118:121], v[22:25]
	v_mfma_f32_16x16x32_f16 v[26:29], v[126:129], v[118:121], v[26:29]
	v_mfma_f32_16x16x32_f16 v[30:33], v[130:133], v[118:121], v[30:33]
	v_mfma_f32_16x16x32_f16 v[38:41], v[122:125], v[134:137], v[38:41]
	v_mfma_f32_16x16x32_f16 v[42:45], v[110:113], v[134:137], v[42:45]
	v_mfma_f32_16x16x32_f16 v[50:53], v[126:129], v[134:137], v[50:53]
	v_mfma_f32_16x16x32_f16 v[46:49], v[130:133], v[134:137], v[46:49]
	v_mfma_f32_16x16x32_f16 v[54:57], v[122:125], v[94:97], v[54:57]
	v_mfma_f32_16x16x32_f16 v[58:61], v[110:113], v[94:97], v[58:61]
	v_mfma_f32_16x16x32_f16 v[62:65], v[126:129], v[94:97], v[62:65]
	v_mfma_f32_16x16x32_f16 v[66:69], v[130:133], v[94:97], v[66:69]
	s_waitcnt lgkmcnt(0)
	v_mfma_f32_16x16x32_f16 v[70:73], v[122:125], v[90:93], v[70:73]
	v_mfma_f32_16x16x32_f16 v[74:77], v[110:113], v[90:93], v[74:77]
	v_mfma_f32_16x16x32_f16 v[34:37], v[126:129], v[90:93], v[34:37]
	v_mfma_f32_16x16x32_f16 v[78:81], v[130:133], v[90:93], v[78:81]
	ds_read_b128 v[90:93], v106 offset:16384
	ds_read_b128 v[98:101], v106 offset:18432
	ds_read_b128 v[94:97], v87
	s_waitcnt lgkmcnt(0)
	v_mfma_f32_16x16x32_f16 v[18:21], v[90:93], v[94:97], v[18:21]
	ds_read_b128 v[102:105], v106 offset:20480
	v_mfma_f32_16x16x32_f16 v[22:25], v[98:101], v[94:97], v[22:25]
	ds_read_b128 v[106:109], v106 offset:22528
	s_waitcnt lgkmcnt(0)
	v_mfma_f32_16x16x32_f16 v[26:29], v[102:105], v[94:97], v[26:29]
	ds_read_b128 v[110:113], v87 offset:2048
	v_mfma_f32_16x16x32_f16 v[30:33], v[106:109], v[94:97], v[30:33]
	ds_read_b128 v[94:97], v87 offset:4096
	s_waitcnt lgkmcnt(0)
	v_mfma_f32_16x16x32_f16 v[38:41], v[90:93], v[110:113], v[38:41]
	ds_read_b128 v[114:117], v87 offset:6144
	v_add_u32_e32 v87, v89, v85
	v_mfma_f32_16x16x32_f16 v[42:45], v[98:101], v[110:113], v[42:45]
	ds_read_b128 v[118:121], v87
	v_mfma_f32_16x16x32_f16 v[50:53], v[102:105], v[110:113], v[50:53]
	ds_read_b128 v[122:125], v1 offset:16384
	v_mfma_f32_16x16x32_f16 v[46:49], v[106:109], v[110:113], v[46:49]
	ds_read_b128 v[110:113], v1 offset:18432
	v_mfma_f32_16x16x32_f16 v[126:129], v[90:93], v[94:97], v[54:57]
	ds_read_b128 v[130:133], v1 offset:20480
	v_mfma_f32_16x16x32_f16 v[134:137], v[98:101], v[94:97], v[58:61]
	ds_read_b128 v[138:141], v1 offset:22528
	v_mov_b32_e32 v1, 0
	v_lshl_add_u64 v[0:1], s[0:1], 0, v[0:1]
	v_mfma_f32_16x16x32_f16 v[142:145], v[102:105], v[94:97], v[62:65]
	ds_read_b128 v[146:149], v87 offset:2048
	v_mfma_f32_16x16x32_f16 v[94:97], v[106:109], v[94:97], v[66:69]
	ds_read_b128 v[150:153], v87 offset:4096
	s_waitcnt lgkmcnt(0)
	v_mfma_f32_16x16x32_f16 v[90:93], v[90:93], v[114:117], v[70:73]
	ds_read_b128 v[154:157], v87 offset:6144
	v_mfma_f32_16x16x32_f16 v[98:101], v[98:101], v[114:117], v[74:77]
	v_mfma_f32_16x16x32_f16 v[102:105], v[102:105], v[114:117], v[34:37]
	v_mfma_f32_16x16x32_f16 v[106:109], v[106:109], v[114:117], v[78:81]
	v_mfma_f32_16x16x32_f16 v[78:81], v[122:125], v[118:121], v[18:21]
	v_mfma_f32_16x16x32_f16 v[74:77], v[110:113], v[118:121], v[22:25]
	v_mfma_f32_16x16x32_f16 v[70:73], v[130:133], v[118:121], v[26:29]
	v_mfma_f32_16x16x32_f16 v[66:69], v[138:141], v[118:121], v[30:33]
	v_mfma_f32_16x16x32_f16 v[62:65], v[122:125], v[146:149], v[38:41]
	v_mfma_f32_16x16x32_f16 v[58:61], v[110:113], v[146:149], v[42:45]
	v_mfma_f32_16x16x32_f16 v[54:57], v[130:133], v[146:149], v[50:53]
	v_mfma_f32_16x16x32_f16 v[50:53], v[138:141], v[146:149], v[46:49]
	v_mfma_f32_16x16x32_f16 v[46:49], v[122:125], v[150:153], v[126:129]
	v_mfma_f32_16x16x32_f16 v[42:45], v[110:113], v[150:153], v[134:137]
	v_mfma_f32_16x16x32_f16 v[38:41], v[130:133], v[150:153], v[142:145]
	v_mfma_f32_16x16x32_f16 v[34:37], v[138:141], v[150:153], v[94:97]
	s_waitcnt lgkmcnt(0)
	v_mfma_f32_16x16x32_f16 v[26:29], v[122:125], v[154:157], v[90:93]
	v_mfma_f32_16x16x32_f16 v[22:25], v[110:113], v[154:157], v[98:101]
	v_mfma_f32_16x16x32_f16 v[18:21], v[130:133], v[154:157], v[102:105]
	v_mfma_f32_16x16x32_f16 v[30:33], v[138:141], v[154:157], v[106:109]
	v_mbcnt_lo_u32_b32 v158, -1, 0
	v_mbcnt_hi_u32_b32 v158, -1, v158
	v_and_b32_e32 v159, 15, v158
	v_lshrrev_b32_e32 v160, 4, v158
	s_lshl_b32 s36, s23, 2
	s_add_u32 s36, s36, s22
	s_mulk_i32 s36, 0x900
	s_add_u32 s36, s36, 0x18000
	v_mul_u32_u24_e32 v161, 0x90, v159
	v_lshl_add_u32 v161, v160, 3, v161
	v_add_u32_e32 v161, s36, v161
	v_lshrrev_b32_e32 v162, 3, v158
	v_and_b32_e32 v163, 7, v158
	v_mul_u32_u24_e32 v164, 0x90, v162
	v_lshl_add_u32 v164, v163, 4, v164
	v_add_u32_e32 v164, s36, v164
	v_lshlrev_b32_e32 v165, 2, v162
	v_add_u32_e32 v166, 32, v165
	v_lshlrev_b32_e32 v182, 4, v163
	v_mov_b32_e32 v183, 0
	s_lshl_b32 s37, s23, 6
	v_add_u32_e32 v167, s37, v162
	s_mov_b64 s[0:1], exec
	s_cbranch_execz .LBB2_8
	s_waitcnt vmcnt(0)
	v_add_f32_e32 v79, v15, v79
	v_ashrrev_i32_e32 v89, 31, v88
	v_add_f32_e32 v78, v14, v78
	v_max_f32_e32 v85, 0, v79
	v_add_f32_e32 v79, v16, v80
	v_add_f32_e32 v80, v17, v81
	v_lshlrev_b64 v[88:89], 11, v[88:89]
	v_max_f32_e32 v78, 0, v78
	v_max_f32_e32 v79, 0, v79
	v_max_f32_e32 v80, 0, v80
	v_lshl_add_u64 v[88:89], v[0:1], 0, v[88:89]
	v_cvt_pk_f16_f32 v79, v79, v80
	v_cvt_pk_f16_f32 v78, v78, v85
	v_add_f32_e32 v75, v11, v75
	ds_write_b64 v161, v[78:79]
	v_add_f32_e32 v74, v10, v74
	v_max_f32_e32 v78, 0, v75
	v_add_f32_e32 v75, v12, v76
	v_add_f32_e32 v76, v13, v77
	v_max_f32_e32 v74, 0, v74
	v_max_f32_e32 v75, 0, v75
	v_max_f32_e32 v76, 0, v76
	v_cvt_pk_f16_f32 v75, v75, v76
	v_cvt_pk_f16_f32 v74, v74, v78
	v_add_f32_e32 v71, v7, v71
	ds_write_b64 v161, v[74:75] offset:32
	v_add_f32_e32 v70, v6, v70
	v_max_f32_e32 v74, 0, v71
	v_add_f32_e32 v71, v8, v72
	v_add_f32_e32 v72, v9, v73
	v_max_f32_e32 v70, 0, v70
	v_max_f32_e32 v71, 0, v71
	v_max_f32_e32 v72, 0, v72
	v_cvt_pk_f16_f32 v71, v71, v72
	v_cvt_pk_f16_f32 v70, v70, v74
	v_add_f32_e32 v67, v3, v67
	ds_write_b64 v161, v[70:71] offset:64
	v_add_f32_e32 v66, v2, v66
	v_max_f32_e32 v70, 0, v67
	v_add_f32_e32 v67, v4, v68
	v_add_f32_e32 v68, v5, v69
	v_max_f32_e32 v66, 0, v66
	v_max_f32_e32 v67, 0, v67
	v_max_f32_e32 v68, 0, v68
	v_cvt_pk_f16_f32 v67, v67, v68
	v_cvt_pk_f16_f32 v66, v66, v70
	ds_write_b64 v161, v[66:67] offset:96
	s_waitcnt lgkmcnt(0)
	ds_read_b128 v[170:173], v164
	ds_read_b128 v[174:177], v164 offset:1152
	ds_bpermute_b32 v178, v165, v88
	ds_bpermute_b32 v179, v165, v89
	ds_bpermute_b32 v180, v166, v88
	ds_bpermute_b32 v181, v166, v89
	v_add_u32_e32 v184, 0, v167
	v_cmp_gt_u32_e64 s[38:39], s2, v184
	v_add_u32_e32 v184, 8, v184
	v_cmp_gt_u32_e64 s[40:41], s2, v184
	s_waitcnt lgkmcnt(0)
	v_lshl_add_u64 v[178:179], v[178:179], 0, v[182:183]
	v_lshl_add_u64 v[180:181], v[180:181], 0, v[182:183]
	s_mov_b64 s[42:43], exec
	s_and_b64 exec, s[42:43], s[38:39]
	global_store_dwordx4 v[178:179], v[170:173], off
	s_and_b64 exec, s[42:43], s[40:41]
	global_store_dwordx4 v[180:181], v[174:177], off
	s_mov_b64 exec, s[42:43]
.LBB2_8:
	s_or_b64 exec, exec, s[0:1]
	v_or_b32_e32 v66, 16, v83
	v_cmp_gt_u32_e32 vcc, s2, v66
	s_mov_b64 s[0:1], exec
	s_cbranch_execz .LBB2_10
	s_waitcnt vmcnt(0)
	v_add_f32_e32 v63, v15, v63
	v_ashrrev_i32_e32 v87, 31, v86
	v_add_f32_e32 v62, v14, v62
	v_max_f32_e32 v68, 0, v63
	v_add_f32_e32 v63, v16, v64
	v_add_f32_e32 v64, v17, v65
	v_lshlrev_b64 v[66:67], 11, v[86:87]
	v_max_f32_e32 v62, 0, v62
	v_max_f32_e32 v63, 0, v63
	v_max_f32_e32 v64, 0, v64
	v_lshl_add_u64 v[66:67], v[0:1], 0, v[66:67]
	v_cvt_pk_f16_f32 v63, v63, v64
	v_cvt_pk_f16_f32 v62, v62, v68
	v_add_f32_e32 v59, v11, v59
	ds_write_b64 v161, v[62:63]
	v_add_f32_e32 v58, v10, v58
	v_max_f32_e32 v62, 0, v59
	v_add_f32_e32 v59, v12, v60
	v_add_f32_e32 v60, v13, v61
	v_max_f32_e32 v58, 0, v58
	v_max_f32_e32 v59, 0, v59
	v_max_f32_e32 v60, 0, v60
	v_cvt_pk_f16_f32 v59, v59, v60
	v_cvt_pk_f16_f32 v58, v58, v62
	v_add_f32_e32 v55, v7, v55
	ds_write_b64 v161, v[58:59] offset:32
	v_add_f32_e32 v54, v6, v54
	v_max_f32_e32 v58, 0, v55
	v_add_f32_e32 v55, v8, v56
	v_add_f32_e32 v56, v9, v57
	v_max_f32_e32 v54, 0, v54
	v_max_f32_e32 v55, 0, v55
	v_max_f32_e32 v56, 0, v56
	v_cvt_pk_f16_f32 v55, v55, v56
	v_cvt_pk_f16_f32 v54, v54, v58
	v_add_f32_e32 v51, v3, v51
	ds_write_b64 v161, v[54:55] offset:64
	v_add_f32_e32 v50, v2, v50
	v_max_f32_e32 v54, 0, v51
	v_add_f32_e32 v51, v4, v52
	v_add_f32_e32 v52, v5, v53
	v_max_f32_e32 v50, 0, v50
	v_max_f32_e32 v51, 0, v51
	v_max_f32_e32 v52, 0, v52
	v_cvt_pk_f16_f32 v51, v51, v52
	v_cvt_pk_f16_f32 v50, v50, v54
	ds_write_b64 v161, v[50:51] offset:96
	s_waitcnt lgkmcnt(0)
	ds_read_b128 v[170:173], v164
	ds_read_b128 v[174:177], v164 offset:1152
	ds_bpermute_b32 v178, v165, v66
	ds_bpermute_b32 v179, v165, v67
	ds_bpermute_b32 v180, v166, v66
	ds_bpermute_b32 v181, v166, v67
	v_add_u32_e32 v184, 16, v167
	v_cmp_gt_u32_e64 s[38:39], s2, v184
	v_add_u32_e32 v184, 8, v184
	v_cmp_gt_u32_e64 s[40:41], s2, v184
	s_waitcnt lgkmcnt(0)
	v_lshl_add_u64 v[178:179], v[178:179], 0, v[182:183]
	v_lshl_add_u64 v[180:181], v[180:181], 0, v[182:183]
	s_mov_b64 s[42:43], exec
	s_and_b64 exec, s[42:43], s[38:39]
	global_store_dwordx4 v[178:179], v[170:173], off
	s_and_b64 exec, s[42:43], s[40:41]
	global_store_dwordx4 v[180:181], v[174:177], off
	s_mov_b64 exec, s[42:43]
.LBB2_10:
	s_or_b64 exec, exec, s[0:1]
	v_or_b32_e32 v50, 32, v83
	v_cmp_gt_u32_e32 vcc, s2, v50
	s_mov_b64 s[0:1], exec
	s_cbranch_execz .LBB2_12
	s_waitcnt vmcnt(0)
	v_add_f32_e32 v47, v15, v47
	v_ashrrev_i32_e32 v85, 31, v84
	v_add_f32_e32 v46, v14, v46
	v_max_f32_e32 v52, 0, v47
	v_add_f32_e32 v47, v16, v48
	v_add_f32_e32 v48, v17, v49
	v_lshlrev_b64 v[50:51], 11, v[84:85]
	v_max_f32_e32 v46, 0, v46
	v_max_f32_e32 v47, 0, v47
	v_max_f32_e32 v48, 0, v48
	v_lshl_add_u64 v[50:51], v[0:1], 0, v[50:51]
	v_cvt_pk_f16_f32 v47, v47, v48
	v_cvt_pk_f16_f32 v46, v46, v52
	v_add_f32_e32 v43, v11, v43
	ds_write_b64 v161, v[46:47]
	v_add_f32_e32 v42, v10, v42
	v_max_f32_e32 v46, 0, v43
	v_add_f32_e32 v43, v12, v44
	v_add_f32_e32 v44, v13, v45
	v_max_f32_e32 v42, 0, v42
	v_max_f32_e32 v43, 0, v43
	v_max_f32_e32 v44, 0, v44
	v_cvt_pk_f16_f32 v43, v43, v44
	v_cvt_pk_f16_f32 v42, v42, v46
	v_add_f32_e32 v39, v7, v39
	ds_write_b64 v161, v[42:43] offset:32
	v_add_f32_e32 v38, v6, v38
	v_max_f32_e32 v42, 0, v39
	v_add_f32_e32 v39, v8, v40
	v_add_f32_e32 v40, v9, v41
	v_max_f32_e32 v38, 0, v38
	v_max_f32_e32 v39, 0, v39
	v_max_f32_e32 v40, 0, v40
	v_cvt_pk_f16_f32 v39, v39, v40
	v_cvt_pk_f16_f32 v38, v38, v42
	v_add_f32_e32 v35, v3, v35
	ds_write_b64 v161, v[38:39] offset:64
	v_add_f32_e32 v34, v2, v34
	v_max_f32_e32 v38, 0, v35
	v_add_f32_e32 v35, v4, v36
	v_add_f32_e32 v36, v5, v37
	v_max_f32_e32 v34, 0, v34
	v_max_f32_e32 v35, 0, v35
	v_max_f32_e32 v36, 0, v36
	v_cvt_pk_f16_f32 v35, v35, v36
	v_cvt_pk_f16_f32 v34, v34, v38
	ds_write_b64 v161, v[34:35] offset:96
	s_waitcnt lgkmcnt(0)
	ds_read_b128 v[170:173], v164
	ds_read_b128 v[174:177], v164 offset:1152
	ds_bpermute_b32 v178, v165, v50
	ds_bpermute_b32 v179, v165, v51
	ds_bpermute_b32 v180, v166, v50
	ds_bpermute_b32 v181, v166, v51
	v_add_u32_e32 v184, 32, v167
	v_cmp_gt_u32_e64 s[38:39], s2, v184
	v_add_u32_e32 v184, 8, v184
	v_cmp_gt_u32_e64 s[40:41], s2, v184
	s_waitcnt lgkmcnt(0)
	v_lshl_add_u64 v[178:179], v[178:179], 0, v[182:183]
	v_lshl_add_u64 v[180:181], v[180:181], 0, v[182:183]
	s_mov_b64 s[42:43], exec
	s_and_b64 exec, s[42:43], s[38:39]
	global_store_dwordx4 v[178:179], v[170:173], off
	s_and_b64 exec, s[42:43], s[40:41]
	global_store_dwordx4 v[180:181], v[174:177], off
	s_mov_b64 exec, s[42:43]
.LBB2_12:
	s_or_b64 exec, exec, s[0:1]
	v_or_b32_e32 v34, 48, v83
	v_cmp_gt_u32_e32 vcc, s2, v34
	s_mov_b64 s[0:1], exec
	s_cbranch_execz .LBB2_14
	s_waitcnt vmcnt(0)
	v_add_f32_e32 v15, v15, v27
	v_ashrrev_i32_e32 v83, 31, v82
	v_add_f32_e32 v14, v14, v26
	v_max_f32_e32 v26, 0, v15
	v_add_f32_e32 v15, v16, v28
	v_add_f32_e32 v16, v17, v29
	v_lshlrev_b64 v[34:35], 11, v[82:83]
	v_max_f32_e32 v14, 0, v14
	v_max_f32_e32 v15, 0, v15
	v_max_f32_e32 v16, 0, v16
	v_lshl_add_u64 v[0:1], v[0:1], 0, v[34:35]
	v_cvt_pk_f16_f32 v15, v15, v16
	v_cvt_pk_f16_f32 v14, v14, v26
	v_add_f32_e32 v11, v11, v23
	ds_write_b64 v161, v[14:15]
	v_add_f32_e32 v10, v10, v22
	v_max_f32_e32 v14, 0, v11
	v_add_f32_e32 v11, v12, v24
	v_add_f32_e32 v12, v13, v25
	v_max_f32_e32 v10, 0, v10
	v_max_f32_e32 v11, 0, v11
	v_max_f32_e32 v12, 0, v12
	v_cvt_pk_f16_f32 v11, v11, v12
	v_cvt_pk_f16_f32 v10, v10, v14
	v_add_f32_e32 v7, v7, v19
	ds_write_b64 v161, v[10:11] offset:32
	v_add_f32_e32 v6, v6, v18
	v_max_f32_e32 v10, 0, v7
	v_add_f32_e32 v7, v8, v20
	v_add_f32_e32 v8, v9, v21
	v_max_f32_e32 v6, 0, v6
	v_max_f32_e32 v7, 0, v7
	v_max_f32_e32 v8, 0, v8
	v_cvt_pk_f16_f32 v7, v7, v8
	v_cvt_pk_f16_f32 v6, v6, v10
	v_add_f32_e32 v3, v3, v31
	ds_write_b64 v161, v[6:7] offset:64
	v_add_f32_e32 v2, v2, v30
	v_max_f32_e32 v6, 0, v3
	v_add_f32_e32 v3, v4, v32
	v_add_f32_e32 v4, v5, v33
	v_max_f32_e32 v2, 0, v2
	v_max_f32_e32 v3, 0, v3
	v_max_f32_e32 v4, 0, v4
	v_cvt_pk_f16_f32 v3, v3, v4
	v_cvt_pk_f16_f32 v2, v2, v6
	ds_write_b64 v161, v[2:3] offset:96
	s_waitcnt lgkmcnt(0)
	ds_read_b128 v[170:173], v164
	ds_read_b128 v[174:177], v164 offset:1152
	ds_bpermute_b32 v178, v165, v0
	ds_bpermute_b32 v179, v165, v1
	ds_bpermute_b32 v180, v166, v0
	ds_bpermute_b32 v181, v166, v1
	v_add_u32_e32 v184, 48, v167
	v_cmp_gt_u32_e64 s[38:39], s2, v184
	v_add_u32_e32 v184, 8, v184
	v_cmp_gt_u32_e64 s[40:41], s2, v184
	s_waitcnt lgkmcnt(0)
	v_lshl_add_u64 v[178:179], v[178:179], 0, v[182:183]
	v_lshl_add_u64 v[180:181], v[180:181], 0, v[182:183]
	s_mov_b64 s[42:43], exec
	s_and_b64 exec, s[42:43], s[38:39]
	global_store_dwordx4 v[178:179], v[170:173], off
	s_and_b64 exec, s[42:43], s[40:41]
	global_store_dwordx4 v[180:181], v[174:177], off
	s_mov_b64 exec, s[42:43]

	.amdhsa_kernel _Z16gemm_glds_kernelILi2EEvPKDF16_PDF16_PKiS4_S1_S1_PKfiS6_Pc
		.amdhsa_group_segment_fixed_size 0
		.amdhsa_private_segment_fixed_size 0
		.amdhsa_kernarg_size 80
		.amdhsa_user_sgpr_count 2
		.amdhsa_user_sgpr_dispatch_ptr 0
		.amdhsa_user_sgpr_queue_ptr 0
		.amdhsa_user_sgpr_kernarg_segment_ptr 1
		.amdhsa_user_sgpr_dispatch_id 0
		.amdhsa_user_sgpr_kernarg_preload_length 0
		.amdhsa_user_sgpr_kernarg_preload_offset 0
		.amdhsa_user_sgpr_private_segment_size 0
		.amdhsa_uses_dynamic_stack 0
		.amdhsa_enable_private_segment 0
		.amdhsa_system_sgpr_workgroup_id_x 1
		.amdhsa_system_sgpr_workgroup_id_y 0
		.amdhsa_system_sgpr_workgroup_id_z 0
		.amdhsa_system_sgpr_workgroup_info 0
		.amdhsa_system_vgpr_workitem_id 0
		.amdhsa_next_free_vgpr 186
		.amdhsa_next_free_sgpr 44
		.amdhsa_accum_offset 188
		.amdhsa_reserve_vcc 1
		.amdhsa_float_round_mode_32 0
		.amdhsa_float_round_mode_16_64 0
		.amdhsa_float_denorm_mode_32 3
		.amdhsa_float_denorm_mode_16_64 3
		.amdhsa_dx10_clamp 1
		.amdhsa_ieee_mode 1
		.amdhsa_fp16_overflow 0
		.amdhsa_tg_split 0
		.amdhsa_exception_fp_ieee_invalid_op 0
		.amdhsa_exception_fp_denorm_src 0
		.amdhsa_exception_fp_ieee_div_zero 0
		.amdhsa_exception_fp_ieee_overflow 0
		.amdhsa_exception_fp_ieee_underflow 0
		.amdhsa_exception_fp_ieee_inexact 0
		.amdhsa_exception_int_div_zero 0
	.end_amdhsa_kernel

_Z11gemm_kernelILi0ELi192ELi256ELi128ELi2ELi4ELi2ELi2ELi64EEvPKDF16_PDF16_PKiS4_S1_S1_PKf:
	s_load_dwordx2 s[4:5], s[0:1], 0x18
	s_waitcnt lgkmcnt(0)
	s_load_dword s3, s[4:5], 0x7fc
	s_waitcnt lgkmcnt(0)
	s_lshl_b32 s6, s3, 3
	s_add_i32 s6, s6, 56
	s_andn2_b32 s6, s6, 63
	s_cmp_ge_i32 s2, s6
	s_cbranch_scc0 .LBB3_2
	s_sub_i32 s6, s2, s6
	s_lshr_b32 s6, s6, 2
	s_and_b32 s7, s2, 7
	s_and_b32 s6, s6, 0x3ffffff8
	s_add_i32 s7, s3, s7
	s_bfe_u32 s19, s2, 0x20003
	s_add_i32 s6, s7, s6
	s_mov_b64 s[8:9], -1
	s_cbranch_execz .LBB3_3
	s_branch .LBB3_4

.LBB3_38:
	ds_read_b128 v[6:9], v196 offset:49152
	ds_read_b128 v[18:21], v196 offset:51200
	ds_read_b128 v[34:37], v194
	ds_read_b128 v[150:153], v194 offset:2048
	ds_read_b128 v[154:157], v196 offset:53248
	ds_read_b128 v[158:161], v196 offset:55296
	s_waitcnt vmcnt(6)
	v_pk_add_f16 v2, v30, v2
	s_waitcnt lgkmcnt(3)
	v_mfma_f32_16x16x32_f16 v[106:109], v[6:9], v[34:37], v[106:109]
	v_pk_add_f16 v3, v31, v3
	v_pk_add_f16 v4, v32, v4
	v_pk_add_f16 v5, v33, v5
	v_mfma_f32_16x16x32_f16 v[102:105], v[18:21], v[34:37], v[102:105]
	v_cndmask_b32_e64 v5, v33, v5, s[2:3]
	v_cndmask_b32_e64 v4, v32, v4, s[2:3]
	v_cndmask_b32_e64 v3, v31, v3, s[2:3]
	s_waitcnt lgkmcnt(1)
	v_mfma_f32_16x16x32_f16 v[98:101], v[154:157], v[34:37], v[98:101]
	v_cndmask_b32_e64 v2, v30, v2, s[2:3]
	v_cmp_gt_u32_e32 vcc, s18, v184
	s_waitcnt lgkmcnt(0)
	v_mfma_f32_16x16x32_f16 v[34:37], v[158:161], v[34:37], v[94:97]
	v_mfma_f32_16x16x32_f16 v[90:93], v[6:9], v[150:153], v[90:93]
	v_mfma_f32_16x16x32_f16 v[86:89], v[18:21], v[150:153], v[86:89]
	v_mfma_f32_16x16x32_f16 v[82:85], v[154:157], v[150:153], v[82:85]
	v_mfma_f32_16x16x32_f16 v[78:81], v[158:161], v[150:153], v[78:81]
	ds_read_b128 v[94:97], v194 offset:4096
	ds_read_b128 v[150:153], v194 offset:6144
	s_waitcnt lgkmcnt(1)
	v_mfma_f32_16x16x32_f16 v[62:65], v[6:9], v[94:97], v[62:65]
	v_mfma_f32_16x16x32_f16 v[58:61], v[18:21], v[94:97], v[58:61]
	v_mfma_f32_16x16x32_f16 v[54:57], v[154:157], v[94:97], v[54:57]
	v_mfma_f32_16x16x32_f16 v[74:77], v[158:161], v[94:97], v[74:77]
	s_waitcnt lgkmcnt(0)
	v_mfma_f32_16x16x32_f16 v[66:69], v[6:9], v[150:153], v[66:69]
	v_mfma_f32_16x16x32_f16 v[70:73], v[18:21], v[150:153], v[70:73]
	v_mfma_f32_16x16x32_f16 v[94:97], v[154:157], v[150:153], v[110:113]
	v_mfma_f32_16x16x32_f16 v[110:113], v[158:161], v[150:153], v[114:117]
	s_nop 2
	ds_read_b128 v[114:117], v194 offset:8192
	ds_read_b128 v[150:153], v194 offset:10240
	s_waitcnt lgkmcnt(1)
	v_mfma_f32_16x16x32_f16 v[118:121], v[6:9], v[114:117], v[118:121]
	v_mfma_f32_16x16x32_f16 v[122:125], v[18:21], v[114:117], v[122:125]
	v_mfma_f32_16x16x32_f16 v[126:129], v[154:157], v[114:117], v[126:129]
	v_mfma_f32_16x16x32_f16 v[114:117], v[158:161], v[114:117], v[130:133]
	s_waitcnt lgkmcnt(0)
	v_mfma_f32_16x16x32_f16 v[6:9], v[6:9], v[150:153], v[134:137]
	v_mfma_f32_16x16x32_f16 v[18:21], v[18:21], v[150:153], v[138:141]
	s_nop 1
	ds_read_b128 v[134:137], v197 offset:49152
	v_mfma_f32_16x16x32_f16 v[130:133], v[154:157], v[150:153], v[146:149]
	v_mfma_f32_16x16x32_f16 v[138:141], v[158:161], v[150:153], v[142:145]
	s_nop 2
	ds_read_b128 v[142:145], v197 offset:51200
	ds_read_b128 v[146:149], v195
	ds_read_b128 v[150:153], v195 offset:2048
	ds_read_b128 v[154:157], v197 offset:53248
	ds_read_b128 v[158:161], v197 offset:55296
	s_waitcnt lgkmcnt(3)
	v_mfma_f32_16x16x32_f16 v[106:109], v[134:137], v[146:149], v[106:109]
	v_mfma_f32_16x16x32_f16 v[102:105], v[142:145], v[146:149], v[102:105]
	s_waitcnt lgkmcnt(1)
	v_mfma_f32_16x16x32_f16 v[98:101], v[154:157], v[146:149], v[98:101]
	s_waitcnt lgkmcnt(0)
	v_mfma_f32_16x16x32_f16 v[34:37], v[158:161], v[146:149], v[34:37]
	v_mfma_f32_16x16x32_f16 v[90:93], v[134:137], v[150:153], v[90:93]
	v_mfma_f32_16x16x32_f16 v[86:89], v[142:145], v[150:153], v[86:89]
	v_mfma_f32_16x16x32_f16 v[82:85], v[154:157], v[150:153], v[82:85]
	v_mfma_f32_16x16x32_f16 v[78:81], v[158:161], v[150:153], v[78:81]
	ds_read_b128 v[146:149], v195 offset:4096
	ds_read_b128 v[150:153], v195 offset:6144
	s_waitcnt lgkmcnt(1)
	v_mfma_f32_16x16x32_f16 v[62:65], v[134:137], v[146:149], v[62:65]
	v_mfma_f32_16x16x32_f16 v[58:61], v[142:145], v[146:149], v[58:61]
	v_mfma_f32_16x16x32_f16 v[54:57], v[154:157], v[146:149], v[54:57]
	v_mfma_f32_16x16x32_f16 v[74:77], v[158:161], v[146:149], v[74:77]
	s_waitcnt lgkmcnt(0)
	v_mfma_f32_16x16x32_f16 v[66:69], v[134:137], v[150:153], v[66:69]
	v_mfma_f32_16x16x32_f16 v[70:73], v[142:145], v[150:153], v[70:73]
	v_mfma_f32_16x16x32_f16 v[94:97], v[154:157], v[150:153], v[94:97]
	v_mfma_f32_16x16x32_f16 v[110:113], v[158:161], v[150:153], v[110:113]
	ds_read_b128 v[146:149], v195 offset:8192
	ds_read_b128 v[150:153], v195 offset:10240
	ds_write_b128 v187, v[2:5] offset:24576
	s_waitcnt vmcnt(5)
	v_pk_add_f16 v2, v26, v10
	v_pk_add_f16 v3, v27, v11
	v_pk_add_f16 v4, v28, v12
	v_pk_add_f16 v5, v29, v13
	v_cndmask_b32_e64 v4, v28, v4, s[2:3]
	v_cndmask_b32_e64 v5, v29, v5, s[2:3]
	v_cndmask_b32_e64 v3, v27, v3, s[2:3]
	v_cndmask_b32_e64 v2, v26, v2, s[2:3]
	ds_write_b128 v187, v[2:5] offset:32768
	s_waitcnt vmcnt(4)
	v_pk_add_f16 v2, v22, v14
	v_pk_add_f16 v3, v23, v15
	v_pk_add_f16 v4, v24, v16
	v_pk_add_f16 v5, v25, v17
	v_cndmask_b32_e64 v4, v24, v4, s[2:3]
	v_cndmask_b32_e64 v5, v25, v5, s[2:3]
	v_cndmask_b32_e64 v3, v23, v3, s[2:3]
	v_cndmask_b32_e64 v2, v22, v2, s[2:3]
	s_waitcnt lgkmcnt(3)
	v_mfma_f32_16x16x32_f16 v[118:121], v[134:137], v[146:149], v[118:121]
	s_lshl_b32 s2, s15, 12
	s_add_u32 s4, s12, s2
	s_addc_u32 s5, s13, 0
	s_waitcnt lgkmcnt(2)
	v_mfma_f32_16x16x32_f16 v[6:9], v[134:137], v[150:153], v[6:9]
	v_add_u32_e32 v134, 0x14000, v187
	ds_write_b128 v187, v[2:5] offset:40960
	s_waitcnt vmcnt(3)
	ds_write_b128 v134, v[38:41]
	s_waitcnt vmcnt(2)
	ds_write_b128 v134, v[42:45] offset:8192
	s_waitcnt vmcnt(1)
	ds_write_b128 v134, v[46:49] offset:16384
	s_waitcnt vmcnt(0)
	ds_write_b128 v134, v[50:53] offset:24576
	s_waitcnt lgkmcnt(0)
	s_barrier
	ds_read_b128 v[2:5], v176 offset:32768
	ds_read_b128 v[14:17], v176 offset:34816
	ds_read_b128 v[22:25], v194 offset:24576
	ds_read_b128 v[26:29], v194 offset:26624
	ds_read_b128 v[38:41], v176 offset:36864
	ds_read_b128 v[46:49], v176 offset:38912
	s_waitcnt lgkmcnt(3)
	v_mfma_f32_16x16x32_f16 v[30:33], v[2:5], v[22:25], v[106:109]
	s_ashr_i32 s15, s14, 31
	s_lshl_b64 s[2:3], s[14:15], 2
	s_add_u32 s2, s4, s2
	v_mfma_f32_16x16x32_f16 v[42:45], v[14:17], v[22:25], v[102:105]
	s_addc_u32 s3, s5, s3
	s_waitcnt lgkmcnt(1)
	v_mfma_f32_16x16x32_f16 v[50:53], v[38:41], v[22:25], v[98:101]
	s_waitcnt lgkmcnt(0)
	v_mfma_f32_16x16x32_f16 v[22:25], v[46:49], v[22:25], v[34:37]
	v_mfma_f32_16x16x32_f16 v[34:37], v[2:5], v[26:29], v[90:93]
	v_mfma_f32_16x16x32_f16 v[86:89], v[14:17], v[26:29], v[86:89]
	v_mfma_f32_16x16x32_f16 v[82:85], v[38:41], v[26:29], v[82:85]
	v_mfma_f32_16x16x32_f16 v[26:29], v[46:49], v[26:29], v[78:81]
	s_nop 2
	ds_read_b128 v[78:81], v194 offset:28672
	ds_read_b128 v[90:93], v194 offset:30720
	v_mfma_f32_16x16x32_f16 v[122:125], v[142:145], v[146:149], v[122:125]
	v_mfma_f32_16x16x32_f16 v[18:21], v[142:145], v[150:153], v[18:21]
	v_mfma_f32_16x16x32_f16 v[10:13], v[158:161], v[150:153], v[138:141]
	s_waitcnt lgkmcnt(0)
	v_mfma_f32_16x16x32_f16 v[138:141], v[2:5], v[90:93], v[66:69]
	v_mfma_f32_16x16x32_f16 v[142:145], v[14:17], v[90:93], v[70:73]
	s_nop 1
	ds_read_b128 v[66:69], v194 offset:32768
	ds_read_b128 v[70:73], v194 offset:34816
	v_mfma_f32_16x16x32_f16 v[126:129], v[154:157], v[146:149], v[126:129]
	v_mfma_f32_16x16x32_f16 v[130:133], v[154:157], v[150:153], v[130:133]
	v_mfma_f32_16x16x32_f16 v[114:117], v[158:161], v[146:149], v[114:117]
	v_mfma_f32_16x16x32_f16 v[62:65], v[2:5], v[78:81], v[62:65]
	v_mfma_f32_16x16x32_f16 v[58:61], v[14:17], v[78:81], v[58:61]
	v_mfma_f32_16x16x32_f16 v[54:57], v[38:41], v[78:81], v[54:57]
	v_mfma_f32_16x16x32_f16 v[146:149], v[38:41], v[90:93], v[94:97]
	s_waitcnt lgkmcnt(1)
	v_mfma_f32_16x16x32_f16 v[118:121], v[2:5], v[66:69], v[118:121]
	v_mfma_f32_16x16x32_f16 v[154:157], v[14:17], v[66:69], v[122:125]
	v_mfma_f32_16x16x32_f16 v[158:161], v[38:41], v[66:69], v[126:129]
	s_waitcnt lgkmcnt(0)
	v_mfma_f32_16x16x32_f16 v[2:5], v[2:5], v[70:73], v[6:9]
	s_nop 0
	v_lshlrev_b32_e32 v126, 2, v184
	v_mov_b32_e32 v129, 0
	v_lshlrev_b32_e32 v128, 8, v186
	v_mfma_f32_16x16x32_f16 v[14:17], v[14:17], v[70:73], v[18:21]
	ds_read_b128 v[6:9], v162 offset:32768
	v_mfma_f32_16x16x32_f16 v[130:133], v[38:41], v[70:73], v[130:133]
	ds_read_b128 v[168:171], v162 offset:34816
	ds_read_b128 v[18:21], v195 offset:24576
	ds_read_b128 v[38:41], v195 offset:26624
	ds_read_b128 v[172:175], v162 offset:36864
	ds_read_b128 v[176:179], v162 offset:38912
	v_mfma_f32_16x16x32_f16 v[134:137], v[46:49], v[78:81], v[74:77]
	v_mfma_f32_16x16x32_f16 v[150:153], v[46:49], v[90:93], v[110:113]
	s_waitcnt lgkmcnt(3)
	v_mfma_f32_16x16x32_f16 v[110:113], v[6:9], v[18:21], v[30:33]
	v_mfma_f32_16x16x32_f16 v[106:109], v[168:171], v[18:21], v[42:45]
	s_waitcnt lgkmcnt(1)
	v_mfma_f32_16x16x32_f16 v[102:105], v[172:175], v[18:21], v[50:53]
	s_waitcnt lgkmcnt(0)
	v_mfma_f32_16x16x32_f16 v[98:101], v[176:179], v[18:21], v[22:25]
	ds_read_b128 v[18:21], v195 offset:28672
	s_nop 1
	ds_read_b128 v[22:25], v195 offset:30720
	v_mfma_f32_16x16x32_f16 v[164:167], v[46:49], v[66:69], v[114:117]
	v_mfma_f32_16x16x32_f16 v[10:13], v[46:49], v[70:73], v[10:13]
	s_waitcnt lgkmcnt(1)
	v_mfma_f32_16x16x32_f16 v[78:81], v[6:9], v[18:21], v[62:65]
	v_mfma_f32_16x16x32_f16 v[74:77], v[168:171], v[18:21], v[58:61]
	v_mfma_f32_16x16x32_f16 v[70:73], v[172:175], v[18:21], v[54:57]
	v_mfma_f32_16x16x32_f16 v[66:69], v[176:179], v[18:21], v[134:137]
	ds_read_b128 v[18:21], v195 offset:32768
	s_nop 1
	ds_read_b128 v[134:137], v195 offset:34816
	s_waitcnt lgkmcnt(1)
	v_mfma_f32_16x16x32_f16 v[46:49], v[6:9], v[18:21], v[118:121]
	global_load_dword v124, v126, s[6:7] offset:64
	global_load_dword v122, v126, s[6:7] offset:128
	s_nop 0
	global_load_dword v120, v126, s[6:7] offset:192
	global_load_dword v118, v126, s[6:7] offset:256
	global_load_dword v114, v126, s[6:7] offset:320
	v_mfma_f32_16x16x32_f16 v[62:65], v[6:9], v[22:25], v[138:141]
	v_mfma_f32_16x16x32_f16 v[58:61], v[168:171], v[22:25], v[142:145]
	v_mfma_f32_16x16x32_f16 v[54:57], v[172:175], v[22:25], v[146:149]
	v_mfma_f32_16x16x32_f16 v[50:53], v[176:179], v[22:25], v[150:153]
	v_lshl_add_u64 v[22:23], s[2:3], 0, v[128:129]
	v_lshlrev_b32_e32 v128, 4, v185
	v_lshl_add_u64 v[22:23], v[22:23], 0, v[128:129]
	v_mfma_f32_16x16x32_f16 v[94:97], v[6:9], v[38:41], v[34:37]
	s_lshl_b64 s[2:3], s[14:15], 1
	s_add_u32 s2, s10, s2
	s_addc_u32 s3, s11, s3
	v_mfma_f32_16x16x32_f16 v[90:93], v[168:171], v[38:41], v[86:89]
	v_lshlrev_b32_e32 v128, 7, v186
	v_lshl_add_u64 v[116:117], s[2:3], 0, v[128:129]
	v_lshlrev_b32_e32 v128, 3, v185
	v_mfma_f32_16x16x32_f16 v[86:89], v[172:175], v[38:41], v[82:85]
	v_lshl_add_u64 v[116:117], v[116:117], 0, v[128:129]
	v_mfma_f32_16x16x32_f16 v[82:85], v[176:179], v[38:41], v[26:29]
	v_mfma_f32_16x16x32_f16 v[42:45], v[168:171], v[18:21], v[154:157]
	v_mfma_f32_16x16x32_f16 v[38:41], v[172:175], v[18:21], v[158:161]
	v_mfma_f32_16x16x32_f16 v[34:37], v[176:179], v[18:21], v[164:167]
	global_load_dwordx4 v[26:29], v[22:23], off
	global_load_dwordx4 v[18:21], v[22:23], off offset:64
	s_waitcnt lgkmcnt(0)
	v_mfma_f32_16x16x32_f16 v[30:33], v[6:9], v[134:137], v[2:5]
	global_load_dwordx4 v[6:9], v[22:23], off offset:128
	s_nop 1
	global_load_dwordx4 v[2:5], v[22:23], off offset:192
	v_mfma_f32_16x16x32_f16 v[22:25], v[168:171], v[134:137], v[14:17]
	v_mfma_f32_16x16x32_f16 v[14:17], v[172:175], v[134:137], v[130:133]
	v_mfma_f32_16x16x32_f16 v[10:13], v[176:179], v[134:137], v[10:13]
	v_mbcnt_lo_u32_b32 v196, -1, 0
	v_mbcnt_hi_u32_b32 v196, -1, v196
	v_and_b32_e32 v197, 15, v196
	v_lshrrev_b32_e32 v198, 4, v196
	v_lshrrev_b32_e32 v222, 10, v187
	s_nop 0
	v_readfirstlane_b32 s36, v222
	s_nop 3
	s_and_b32 s36, s36, 7
	s_mulk_i32 s36, 0x900
	v_mul_u32_u24_e32 v199, 0x90, v197
	v_lshl_add_u32 v199, v198, 3, v199
	v_add_u32_e32 v199, s36, v199
	v_lshrrev_b32_e32 v200, 3, v196
	v_and_b32_e32 v201, 7, v196
	v_mul_u32_u24_e32 v202, 0x90, v200
	v_lshl_add_u32 v202, v201, 4, v202
	v_add_u32_e32 v202, s36, v202
	v_lshlrev_b32_e32 v203, 2, v200
	v_add_u32_e32 v204, 32, v203
	v_lshlrev_b32_e32 v220, 4, v201
	v_mov_b32_e32 v221, 0
	v_sub_u32_e32 v205, v184, v197
	v_add_u32_e32 v205, v205, v200
	s_mov_b64 s[2:3], exec
	s_cbranch_execz .LBB3_40
	v_mov_b32_e32 v127, v129
	v_lshl_add_u64 v[126:127], s[6:7], 0, v[126:127]
	global_load_dword v126, v[126:127], off
	s_waitcnt vmcnt(3)
	v_add_f32_e32 v106, v106, v18
	v_add_f32_e32 v107, v107, v19
	v_add_f32_e32 v110, v110, v26
	v_add_f32_e32 v111, v111, v27
	v_add_f32_e32 v112, v112, v28
	v_add_f32_e32 v113, v113, v29
	s_waitcnt vmcnt(2)
	v_add_f32_e32 v103, v103, v7
	v_add_f32_e32 v104, v104, v8
	v_add_f32_e32 v105, v105, v9
	s_waitcnt vmcnt(1)
	v_add_f32_e32 v100, v100, v4
	v_max_f32_e32 v106, 0, v106
	v_max_f32_e32 v107, 0, v107
	v_add_f32_e32 v108, v108, v20
	v_add_f32_e32 v109, v109, v21
	v_add_f32_e32 v102, v102, v6
	v_add_f32_e32 v98, v98, v2
	v_add_f32_e32 v99, v99, v3
	v_add_f32_e32 v101, v101, v5
	v_max_f32_e32 v110, 0, v110
	v_max_f32_e32 v111, 0, v111
	v_max_f32_e32 v112, 0, v112
	v_max_f32_e32 v113, 0, v113
	v_max_f32_e32 v115, 0, v103
	v_max_f32_e32 v103, 0, v104
	v_max_f32_e32 v104, 0, v105
	v_max_f32_e32 v105, 0, v100
	v_cvt_pk_f16_f32 v100, v106, v107
	v_max_f32_e32 v108, 0, v108
	v_max_f32_e32 v109, 0, v109
	v_max_f32_e32 v102, 0, v102
	v_max_f32_e32 v119, 0, v98
	v_max_f32_e32 v121, 0, v99
	v_max_f32_e32 v123, 0, v101
	v_cvt_pk_f16_f32 v99, v112, v113
	v_cvt_pk_f16_f32 v98, v110, v111
	v_cvt_pk_f16_f32 v101, v108, v109
	v_cvt_pk_f16_f32 v103, v103, v104
	v_cvt_pk_f16_f32 v102, v102, v115
	v_cvt_pk_f16_f32 v105, v105, v123
	v_cvt_pk_f16_f32 v104, v119, v121
	s_waitcnt vmcnt(0)
	v_ashrrev_i32_e32 v127, 31, v126
	v_lshlrev_b64 v[106:107], 11, v[126:127]
	v_lshl_add_u64 v[106:107], v[116:117], 0, v[106:107]
	ds_write_b64 v199, v[98:99]
	ds_write_b64 v199, v[100:101] offset:32
	ds_write_b64 v199, v[102:103] offset:64
	ds_write_b64 v199, v[104:105] offset:96
	s_waitcnt lgkmcnt(0)
	ds_read_b128 v[208:211], v202
	ds_read_b128 v[212:215], v202 offset:1152
	ds_bpermute_b32 v216, v203, v106
	ds_bpermute_b32 v217, v203, v107
	ds_bpermute_b32 v218, v204, v106
	ds_bpermute_b32 v219, v204, v107
	v_add_u32_e32 v222, 0, v205
	v_cmp_gt_u32_e64 s[38:39], s18, v222
	v_add_u32_e32 v222, 8, v222
	v_cmp_gt_u32_e64 s[40:41], s18, v222
	s_waitcnt lgkmcnt(0)
	v_lshl_add_u64 v[216:217], v[216:217], 0, v[220:221]
	v_lshl_add_u64 v[218:219], v[218:219], 0, v[220:221]
	s_mov_b64 s[42:43], exec
	s_and_b64 exec, s[42:43], s[38:39]
	global_store_dwordx4 v[216:217], v[208:211], off
	s_and_b64 exec, s[42:43], s[40:41]
	global_store_dwordx4 v[218:219], v[212:215], off
	s_mov_b64 exec, s[42:43]
.LBB3_40:
	s_or_b64 exec, exec, s[2:3]
	v_or_b32_e32 v98, 16, v184
	v_cmp_gt_u32_e32 vcc, s18, v98
	s_mov_b64 s[2:3], exec
	s_cbranch_execz .LBB3_42
	s_waitcnt vmcnt(3)
	v_add_f32_e32 v95, v95, v27
	v_ashrrev_i32_e32 v125, 31, v124
	v_add_f32_e32 v94, v94, v26
	v_max_f32_e32 v100, 0, v95
	v_add_f32_e32 v95, v96, v28
	v_add_f32_e32 v96, v97, v29
	v_lshlrev_b64 v[98:99], 11, v[124:125]
	v_max_f32_e32 v94, 0, v94
	v_max_f32_e32 v95, 0, v95
	v_max_f32_e32 v96, 0, v96
	v_lshl_add_u64 v[98:99], v[116:117], 0, v[98:99]
	v_cvt_pk_f16_f32 v95, v95, v96
	v_cvt_pk_f16_f32 v94, v94, v100
	s_waitcnt vmcnt(2)
	v_add_f32_e32 v91, v91, v19
	ds_write_b64 v199, v[94:95]
	v_add_f32_e32 v90, v90, v18
	v_max_f32_e32 v94, 0, v91
	v_add_f32_e32 v91, v92, v20
	v_add_f32_e32 v92, v93, v21
	v_max_f32_e32 v90, 0, v90
	v_max_f32_e32 v91, 0, v91
	v_max_f32_e32 v92, 0, v92
	v_cvt_pk_f16_f32 v91, v91, v92
	v_cvt_pk_f16_f32 v90, v90, v94
	s_waitcnt vmcnt(2)
	v_add_f32_e32 v87, v87, v7
	ds_write_b64 v199, v[90:91] offset:32
	v_add_f32_e32 v86, v86, v6
	v_max_f32_e32 v90, 0, v87
	v_add_f32_e32 v87, v88, v8
	v_add_f32_e32 v88, v89, v9
	v_max_f32_e32 v86, 0, v86
	v_max_f32_e32 v87, 0, v87
	v_max_f32_e32 v88, 0, v88
	v_cvt_pk_f16_f32 v87, v87, v88
	v_cvt_pk_f16_f32 v86, v86, v90
	s_waitcnt vmcnt(2)
	v_add_f32_e32 v83, v83, v3
	ds_write_b64 v199, v[86:87] offset:64
	v_add_f32_e32 v82, v82, v2
	v_max_f32_e32 v86, 0, v83
	v_add_f32_e32 v83, v84, v4
	v_add_f32_e32 v84, v85, v5
	v_max_f32_e32 v82, 0, v82
	v_max_f32_e32 v83, 0, v83
	v_max_f32_e32 v84, 0, v84
	v_cvt_pk_f16_f32 v83, v83, v84
	v_cvt_pk_f16_f32 v82, v82, v86
	ds_write_b64 v199, v[82:83] offset:96
	s_waitcnt lgkmcnt(0)
	ds_read_b128 v[208:211], v202
	ds_read_b128 v[212:215], v202 offset:1152
	ds_bpermute_b32 v216, v203, v98
	ds_bpermute_b32 v217, v203, v99
	ds_bpermute_b32 v218, v204, v98
	ds_bpermute_b32 v219, v204, v99
	v_add_u32_e32 v222, 16, v205
	v_cmp_gt_u32_e64 s[38:39], s18, v222
	v_add_u32_e32 v222, 8, v222
	v_cmp_gt_u32_e64 s[40:41], s18, v222
	s_waitcnt lgkmcnt(0)
	v_lshl_add_u64 v[216:217], v[216:217], 0, v[220:221]
	v_lshl_add_u64 v[218:219], v[218:219], 0, v[220:221]
	s_mov_b64 s[42:43], exec
	s_and_b64 exec, s[42:43], s[38:39]
	global_store_dwordx4 v[216:217], v[208:211], off
	s_and_b64 exec, s[42:43], s[40:41]
	global_store_dwordx4 v[218:219], v[212:215], off
	s_mov_b64 exec, s[42:43]
.LBB3_42:
	s_or_b64 exec, exec, s[2:3]
	v_add_u32_e32 v82, 32, v184
	v_cmp_gt_u32_e32 vcc, s18, v82
	s_mov_b64 s[2:3], exec
	s_cbranch_execz .LBB3_44
	s_waitcnt vmcnt(3)
	v_add_f32_e32 v79, v79, v27
	v_ashrrev_i32_e32 v123, 31, v122
	v_add_f32_e32 v78, v78, v26
	v_max_f32_e32 v84, 0, v79
	v_add_f32_e32 v79, v80, v28
	v_add_f32_e32 v80, v81, v29
	v_lshlrev_b64 v[82:83], 11, v[122:123]
	v_max_f32_e32 v78, 0, v78
	v_max_f32_e32 v79, 0, v79
	v_max_f32_e32 v80, 0, v80
	v_lshl_add_u64 v[82:83], v[116:117], 0, v[82:83]
	v_cvt_pk_f16_f32 v79, v79, v80
	v_cvt_pk_f16_f32 v78, v78, v84
	s_waitcnt vmcnt(2)
	v_add_f32_e32 v75, v75, v19
	ds_write_b64 v199, v[78:79]
	v_add_f32_e32 v74, v74, v18
	v_max_f32_e32 v78, 0, v75
	v_add_f32_e32 v75, v76, v20
	v_add_f32_e32 v76, v77, v21
	v_max_f32_e32 v74, 0, v74
	v_max_f32_e32 v75, 0, v75
	v_max_f32_e32 v76, 0, v76
	v_cvt_pk_f16_f32 v75, v75, v76
	v_cvt_pk_f16_f32 v74, v74, v78
	s_waitcnt vmcnt(2)
	v_add_f32_e32 v71, v71, v7
	ds_write_b64 v199, v[74:75] offset:32
	v_add_f32_e32 v70, v70, v6
	v_max_f32_e32 v74, 0, v71
	v_add_f32_e32 v71, v72, v8
	v_add_f32_e32 v72, v73, v9
	v_max_f32_e32 v70, 0, v70
	v_max_f32_e32 v71, 0, v71
	v_max_f32_e32 v72, 0, v72
	v_cvt_pk_f16_f32 v71, v71, v72
	v_cvt_pk_f16_f32 v70, v70, v74
	s_waitcnt vmcnt(2)
	v_add_f32_e32 v67, v67, v3
	ds_write_b64 v199, v[70:71] offset:64
	v_add_f32_e32 v66, v66, v2
	v_max_f32_e32 v70, 0, v67
	v_add_f32_e32 v67, v68, v4
	v_add_f32_e32 v68, v69, v5
	v_max_f32_e32 v66, 0, v66
	v_max_f32_e32 v67, 0, v67
	v_max_f32_e32 v68, 0, v68
	v_cvt_pk_f16_f32 v67, v67, v68
	v_cvt_pk_f16_f32 v66, v66, v70
	ds_write_b64 v199, v[66:67] offset:96
	s_waitcnt lgkmcnt(0)
	ds_read_b128 v[208:211], v202
	ds_read_b128 v[212:215], v202 offset:1152
	ds_bpermute_b32 v216, v203, v82
	ds_bpermute_b32 v217, v203, v83
	ds_bpermute_b32 v218, v204, v82
	ds_bpermute_b32 v219, v204, v83
	v_add_u32_e32 v222, 32, v205
	v_cmp_gt_u32_e64 s[38:39], s18, v222
	v_add_u32_e32 v222, 8, v222
	v_cmp_gt_u32_e64 s[40:41], s18, v222
	s_waitcnt lgkmcnt(0)
	v_lshl_add_u64 v[216:217], v[216:217], 0, v[220:221]
	v_lshl_add_u64 v[218:219], v[218:219], 0, v[220:221]
	s_mov_b64 s[42:43], exec
	s_and_b64 exec, s[42:43], s[38:39]
	global_store_dwordx4 v[216:217], v[208:211], off
	s_and_b64 exec, s[42:43], s[40:41]
	global_store_dwordx4 v[218:219], v[212:215], off
	s_mov_b64 exec, s[42:43]
.LBB3_44:
	s_or_b64 exec, exec, s[2:3]
	v_add_u32_e32 v66, 48, v184
	v_cmp_gt_u32_e32 vcc, s18, v66
	s_mov_b64 s[2:3], exec
	s_cbranch_execz .LBB3_46
	s_waitcnt vmcnt(3)
	v_add_f32_e32 v63, v63, v27
	v_ashrrev_i32_e32 v121, 31, v120
	v_add_f32_e32 v62, v62, v26
	v_max_f32_e32 v68, 0, v63
	v_add_f32_e32 v63, v64, v28
	v_add_f32_e32 v64, v65, v29
	v_lshlrev_b64 v[66:67], 11, v[120:121]
	v_max_f32_e32 v62, 0, v62
	v_max_f32_e32 v63, 0, v63
	v_max_f32_e32 v64, 0, v64
	v_lshl_add_u64 v[66:67], v[116:117], 0, v[66:67]
	v_cvt_pk_f16_f32 v63, v63, v64
	v_cvt_pk_f16_f32 v62, v62, v68
	s_waitcnt vmcnt(2)
	v_add_f32_e32 v59, v59, v19
	ds_write_b64 v199, v[62:63]
	v_add_f32_e32 v58, v58, v18
	v_max_f32_e32 v62, 0, v59
	v_add_f32_e32 v59, v60, v20
	v_add_f32_e32 v60, v61, v21
	v_max_f32_e32 v58, 0, v58
	v_max_f32_e32 v59, 0, v59
	v_max_f32_e32 v60, 0, v60
	v_cvt_pk_f16_f32 v59, v59, v60
	v_cvt_pk_f16_f32 v58, v58, v62
	s_waitcnt vmcnt(2)
	v_add_f32_e32 v55, v55, v7
	ds_write_b64 v199, v[58:59] offset:32
	v_add_f32_e32 v54, v54, v6
	v_max_f32_e32 v58, 0, v55
	v_add_f32_e32 v55, v56, v8
	v_add_f32_e32 v56, v57, v9
	v_max_f32_e32 v54, 0, v54
	v_max_f32_e32 v55, 0, v55
	v_max_f32_e32 v56, 0, v56
	v_cvt_pk_f16_f32 v55, v55, v56
	v_cvt_pk_f16_f32 v54, v54, v58
	s_waitcnt vmcnt(2)
	v_add_f32_e32 v51, v51, v3
	ds_write_b64 v199, v[54:55] offset:64
	v_add_f32_e32 v50, v50, v2
	v_max_f32_e32 v54, 0, v51
	v_add_f32_e32 v51, v52, v4
	v_add_f32_e32 v52, v53, v5
	v_max_f32_e32 v50, 0, v50
	v_max_f32_e32 v51, 0, v51
	v_max_f32_e32 v52, 0, v52
	v_cvt_pk_f16_f32 v51, v51, v52
	v_cvt_pk_f16_f32 v50, v50, v54
	ds_write_b64 v199, v[50:51] offset:96
	s_waitcnt lgkmcnt(0)
	ds_read_b128 v[208:211], v202
	ds_read_b128 v[212:215], v202 offset:1152
	ds_bpermute_b32 v216, v203, v66
	ds_bpermute_b32 v217, v203, v67
	ds_bpermute_b32 v218, v204, v66
	ds_bpermute_b32 v219, v204, v67
	v_add_u32_e32 v222, 48, v205
	v_cmp_gt_u32_e64 s[38:39], s18, v222
	v_add_u32_e32 v222, 8, v222
	v_cmp_gt_u32_e64 s[40:41], s18, v222
	s_waitcnt lgkmcnt(0)
	v_lshl_add_u64 v[216:217], v[216:217], 0, v[220:221]
	v_lshl_add_u64 v[218:219], v[218:219], 0, v[220:221]
	s_mov_b64 s[42:43], exec
	s_and_b64 exec, s[42:43], s[38:39]
	global_store_dwordx4 v[216:217], v[208:211], off
	s_and_b64 exec, s[42:43], s[40:41]
	global_store_dwordx4 v[218:219], v[212:215], off
	s_mov_b64 exec, s[42:43]
.LBB3_46:
	s_or_b64 exec, exec, s[2:3]
	v_add_u32_e32 v50, 64, v184
	v_cmp_gt_u32_e32 vcc, s18, v50
	s_mov_b64 s[2:3], exec
	s_cbranch_execz .LBB3_48
	s_waitcnt vmcnt(3)
	v_add_f32_e32 v47, v47, v27
	v_ashrrev_i32_e32 v119, 31, v118
	v_add_f32_e32 v46, v46, v26
	v_max_f32_e32 v52, 0, v47
	v_add_f32_e32 v47, v48, v28
	v_add_f32_e32 v48, v49, v29
	v_lshlrev_b64 v[50:51], 11, v[118:119]
	v_max_f32_e32 v46, 0, v46
	v_max_f32_e32 v47, 0, v47
	v_max_f32_e32 v48, 0, v48
	v_lshl_add_u64 v[50:51], v[116:117], 0, v[50:51]
	v_cvt_pk_f16_f32 v47, v47, v48
	v_cvt_pk_f16_f32 v46, v46, v52
	s_waitcnt vmcnt(2)
	v_add_f32_e32 v43, v43, v19
	ds_write_b64 v199, v[46:47]
	v_add_f32_e32 v42, v42, v18
	v_max_f32_e32 v46, 0, v43
	v_add_f32_e32 v43, v44, v20
	v_add_f32_e32 v44, v45, v21
	v_max_f32_e32 v42, 0, v42
	v_max_f32_e32 v43, 0, v43
	v_max_f32_e32 v44, 0, v44
	v_cvt_pk_f16_f32 v43, v43, v44
	v_cvt_pk_f16_f32 v42, v42, v46
	s_waitcnt vmcnt(2)
	v_add_f32_e32 v39, v39, v7
	ds_write_b64 v199, v[42:43] offset:32
	v_add_f32_e32 v38, v38, v6
	v_max_f32_e32 v42, 0, v39
	v_add_f32_e32 v39, v40, v8
	v_add_f32_e32 v40, v41, v9
	v_max_f32_e32 v38, 0, v38
	v_max_f32_e32 v39, 0, v39
	v_max_f32_e32 v40, 0, v40
	v_cvt_pk_f16_f32 v39, v39, v40
	v_cvt_pk_f16_f32 v38, v38, v42
	s_waitcnt vmcnt(2)
	v_add_f32_e32 v35, v35, v3
	ds_write_b64 v199, v[38:39] offset:64
	v_add_f32_e32 v34, v34, v2
	v_max_f32_e32 v38, 0, v35
	v_add_f32_e32 v35, v36, v4
	v_add_f32_e32 v36, v37, v5
	v_max_f32_e32 v34, 0, v34
	v_max_f32_e32 v35, 0, v35
	v_max_f32_e32 v36, 0, v36
	v_cvt_pk_f16_f32 v35, v35, v36
	v_cvt_pk_f16_f32 v34, v34, v38
	ds_write_b64 v199, v[34:35] offset:96
	s_waitcnt lgkmcnt(0)
	ds_read_b128 v[208:211], v202
	ds_read_b128 v[212:215], v202 offset:1152
	ds_bpermute_b32 v216, v203, v50
	ds_bpermute_b32 v217, v203, v51
	ds_bpermute_b32 v218, v204, v50
	ds_bpermute_b32 v219, v204, v51
	v_add_u32_e32 v222, 64, v205
	v_cmp_gt_u32_e64 s[38:39], s18, v222
	v_add_u32_e32 v222, 8, v222
	v_cmp_gt_u32_e64 s[40:41], s18, v222
	s_waitcnt lgkmcnt(0)
	v_lshl_add_u64 v[216:217], v[216:217], 0, v[220:221]
	v_lshl_add_u64 v[218:219], v[218:219], 0, v[220:221]
	s_mov_b64 s[42:43], exec
	s_and_b64 exec, s[42:43], s[38:39]
	global_store_dwordx4 v[216:217], v[208:211], off
	s_and_b64 exec, s[42:43], s[40:41]
	global_store_dwordx4 v[218:219], v[212:215], off
	s_mov_b64 exec, s[42:43]
.LBB3_48:
	s_or_b64 exec, exec, s[2:3]
	v_add_u32_e32 v34, 0x50, v184
	v_cmp_gt_u32_e32 vcc, s18, v34
	s_mov_b64 s[2:3], exec
	s_cbranch_execz .LBB3_50
	s_waitcnt vmcnt(1)
	v_add_f32_e32 v7, v15, v7
	v_ashrrev_i32_e32 v115, 31, v114
	v_add_f32_e32 v6, v14, v6
	v_max_f32_e32 v14, 0, v7
	v_add_f32_e32 v7, v16, v8
	v_add_f32_e32 v8, v17, v9
	v_lshlrev_b64 v[34:35], 11, v[114:115]
	v_max_f32_e32 v6, 0, v6
	v_max_f32_e32 v7, 0, v7
	v_max_f32_e32 v8, 0, v8
	v_lshl_add_u64 v[34:35], v[116:117], 0, v[34:35]
	v_add_f32_e32 v27, v31, v27
	v_add_f32_e32 v19, v23, v19
	v_cvt_pk_f16_f32 v7, v7, v8
	v_cvt_pk_f16_f32 v6, v6, v14
	s_waitcnt vmcnt(0)
	v_add_f32_e32 v3, v11, v3
	v_add_f32_e32 v26, v30, v26
	v_max_f32_e32 v30, 0, v27
	v_add_f32_e32 v27, v32, v28
	v_add_f32_e32 v28, v33, v29
	v_add_f32_e32 v18, v22, v18
	v_max_f32_e32 v22, 0, v19
	v_add_f32_e32 v19, v24, v20
	v_add_f32_e32 v20, v25, v21
	ds_write_b64 v199, v[6:7] offset:64
	v_add_f32_e32 v2, v10, v2
	v_max_f32_e32 v6, 0, v3
	v_add_f32_e32 v3, v12, v4
	v_add_f32_e32 v4, v13, v5
	v_max_f32_e32 v26, 0, v26
	v_max_f32_e32 v27, 0, v27
	v_max_f32_e32 v28, 0, v28
	v_max_f32_e32 v18, 0, v18
	v_max_f32_e32 v19, 0, v19
	v_max_f32_e32 v20, 0, v20
	v_max_f32_e32 v2, 0, v2
	v_max_f32_e32 v3, 0, v3
	v_max_f32_e32 v4, 0, v4
	v_cvt_pk_f16_f32 v27, v27, v28
	v_cvt_pk_f16_f32 v26, v26, v30
	v_cvt_pk_f16_f32 v19, v19, v20
	v_cvt_pk_f16_f32 v18, v18, v22
	v_cvt_pk_f16_f32 v3, v3, v4
	v_cvt_pk_f16_f32 v2, v2, v6
	ds_write_b64 v199, v[26:27]
	ds_write_b64 v199, v[18:19] offset:32
	ds_write_b64 v199, v[2:3] offset:96
	s_waitcnt lgkmcnt(0)
	ds_read_b128 v[208:211], v202
	ds_read_b128 v[212:215], v202 offset:1152
	ds_bpermute_b32 v216, v203, v34
	ds_bpermute_b32 v217, v203, v35
	ds_bpermute_b32 v218, v204, v34
	ds_bpermute_b32 v219, v204, v35
	v_add_u32_e32 v222, 80, v205
	v_cmp_gt_u32_e64 s[38:39], s18, v222
	v_add_u32_e32 v222, 8, v222
	v_cmp_gt_u32_e64 s[40:41], s18, v222
	s_waitcnt lgkmcnt(0)
	v_lshl_add_u64 v[216:217], v[216:217], 0, v[220:221]
	v_lshl_add_u64 v[218:219], v[218:219], 0, v[220:221]
	s_mov_b64 s[42:43], exec
	s_and_b64 exec, s[42:43], s[38:39]
	global_store_dwordx4 v[216:217], v[208:211], off
	s_and_b64 exec, s[42:43], s[40:41]
	global_store_dwordx4 v[218:219], v[212:215], off
	s_mov_b64 exec, s[42:43]

.LBB3_53:
	v_add_u32_e32 v104, v81, v83
	v_add_u32_e32 v102, v89, v83
	ds_read_b128 v[106:109], v104 offset:49152
	ds_read_b128 v[110:113], v104 offset:51200
	ds_read_b128 v[114:117], v102
	ds_read_b128 v[118:121], v102 offset:2048
	v_add_u32_e32 v103, v89, v87
	v_add_u32_e32 v105, v81, v87
	s_waitcnt lgkmcnt(1)
	v_mfma_f32_16x16x32_f16 v[46:49], v[106:109], v[114:117], v[46:49]
	v_lshl_add_u64 v[154:155], v[96:97], 0, v[84:85]
	v_lshl_add_u64 v[156:157], v[98:99], 0, v[84:85]
	v_lshl_add_u64 v[160:161], v[94:95], 0, v[84:85]
	v_mfma_f32_16x16x32_f16 v[38:41], v[110:113], v[114:117], v[38:41]
	v_lshl_add_u64 v[158:159], v[100:101], 0, v[84:85]
	v_add_co_u32_e32 v162, vcc, s14, v160
	s_waitcnt lgkmcnt(0)
	v_mfma_f32_16x16x32_f16 v[34:37], v[106:109], v[118:121], v[34:37]
	v_addc_co_u32_e32 v163, vcc, 0, v161, vcc
	s_add_i32 s4, s4, 2
	v_mfma_f32_16x16x32_f16 v[30:33], v[110:113], v[118:121], v[30:33]
	ds_read_b128 v[114:117], v102 offset:4096
	ds_read_b128 v[118:121], v102 offset:6144
	v_lshl_add_u64 v[96:97], v[96:97], 0, s[2:3]
	v_lshl_add_u64 v[98:99], v[98:99], 0, s[2:3]
	s_waitcnt lgkmcnt(1)
	v_mfma_f32_16x16x32_f16 v[42:45], v[106:109], v[114:117], v[42:45]
	v_lshl_add_u64 v[100:101], v[100:101], 0, s[2:3]
	v_lshl_add_u64 v[94:95], v[94:95], 0, s[2:3]
	s_cmp_lt_u32 s4, 27
	v_mfma_f32_16x16x32_f16 v[50:53], v[110:113], v[114:117], v[50:53]
	s_waitcnt lgkmcnt(0)
	v_mfma_f32_16x16x32_f16 v[54:57], v[106:109], v[118:121], v[54:57]
	v_mfma_f32_16x16x32_f16 v[58:61], v[110:113], v[118:121], v[58:61]
	ds_read_b128 v[114:117], v102 offset:8192
	ds_read_b128 v[118:121], v102 offset:10240
	s_waitcnt lgkmcnt(1)
	v_mfma_f32_16x16x32_f16 v[62:65], v[106:109], v[114:117], v[62:65]
	v_mfma_f32_16x16x32_f16 v[66:69], v[110:113], v[114:117], v[66:69]
	ds_read_b128 v[114:117], v105 offset:49152
	ds_read_b128 v[122:125], v105 offset:51200
	s_waitcnt lgkmcnt(2)
	v_mfma_f32_16x16x32_f16 v[74:77], v[106:109], v[118:121], v[74:77]
	v_mfma_f32_16x16x32_f16 v[70:73], v[110:113], v[118:121], v[70:73]
	ds_read_b128 v[106:109], v103
	ds_read_b128 v[110:113], v103 offset:2048
	s_waitcnt lgkmcnt(1)
	v_mfma_f32_16x16x32_f16 v[46:49], v[114:117], v[106:109], v[46:49]
	v_mfma_f32_16x16x32_f16 v[38:41], v[122:125], v[106:109], v[38:41]
	v_add_u32_e32 v106, v93, v83
	v_add_u32_e32 v107, v93, v87
	s_waitcnt lgkmcnt(0)
	v_mfma_f32_16x16x32_f16 v[34:37], v[114:117], v[110:113], v[34:37]
	v_mfma_f32_16x16x32_f16 v[30:33], v[122:125], v[110:113], v[30:33]
	ds_read_b128 v[108:111], v103 offset:4096
	ds_read_b128 v[118:121], v103 offset:6144
	global_load_dwordx4 v[126:129], v[154:155], off offset:256
	ds_read_b128 v[130:133], v103 offset:8192
	ds_read_b128 v[134:137], v103 offset:10240
	s_waitcnt vmcnt(3)
	ds_write_b128 v1, v[26:29] offset:24576
	s_waitcnt lgkmcnt(4)
	v_mfma_f32_16x16x32_f16 v[42:45], v[114:117], v[108:111], v[42:45]
	v_mfma_f32_16x16x32_f16 v[50:53], v[122:125], v[108:111], v[50:53]
	global_load_dwordx4 v[108:111], v[156:157], off offset:256
	global_load_dwordx4 v[138:141], v[158:159], off offset:256
	s_waitcnt vmcnt(4)
	ds_write_b128 v1, v[22:25] offset:32768
	s_waitcnt vmcnt(3)
	ds_write_b128 v1, v[18:21] offset:40960
	ds_write_b128 v91, v[10:13] offset:16384
	ds_write_b128 v91, v[14:17] offset:24576
	s_waitcnt lgkmcnt(7)
	v_mfma_f32_16x16x32_f16 v[26:29], v[114:117], v[118:121], v[54:57]
	v_mfma_f32_16x16x32_f16 v[54:57], v[122:125], v[118:121], v[58:61]
	global_load_dwordx4 v[118:121], v[160:161], off offset:256
	global_load_dwordx4 v[142:145], v[162:163], off offset:256
	s_waitcnt lgkmcnt(0)
	s_barrier
	v_mfma_f32_16x16x32_f16 v[10:13], v[114:117], v[130:133], v[62:65]
	ds_read_b128 v[22:25], v106 offset:16384
	ds_read_b128 v[58:61], v106 offset:18432
	v_mfma_f32_16x16x32_f16 v[14:17], v[122:125], v[130:133], v[66:69]
	v_mfma_f32_16x16x32_f16 v[62:65], v[122:125], v[134:137], v[70:73]
	s_nop 1
	ds_read_b128 v[66:69], v102 offset:24576
	ds_read_b128 v[70:73], v102 offset:26624
	s_waitcnt lgkmcnt(1)
	v_mfma_f32_16x16x32_f16 v[46:49], v[22:25], v[66:69], v[46:49]
	v_mfma_f32_16x16x32_f16 v[38:41], v[58:61], v[66:69], v[38:41]
	s_waitcnt lgkmcnt(0)
	v_mfma_f32_16x16x32_f16 v[34:37], v[22:25], v[70:73], v[34:37]
	v_mfma_f32_16x16x32_f16 v[30:33], v[58:61], v[70:73], v[30:33]
	ds_read_b128 v[66:69], v102 offset:28672
	ds_read_b128 v[70:73], v102 offset:30720
	s_waitcnt lgkmcnt(1)
	v_mfma_f32_16x16x32_f16 v[42:45], v[22:25], v[66:69], v[42:45]
	v_mfma_f32_16x16x32_f16 v[50:53], v[58:61], v[66:69], v[50:53]
	s_waitcnt lgkmcnt(0)
	v_mfma_f32_16x16x32_f16 v[26:29], v[22:25], v[70:73], v[26:29]
	v_mfma_f32_16x16x32_f16 v[66:69], v[58:61], v[70:73], v[54:57]
	s_nop 2
	ds_read_b128 v[54:57], v102 offset:32768
	ds_read_b128 v[70:73], v102 offset:34816
	v_mfma_f32_16x16x32_f16 v[18:21], v[114:117], v[134:137], v[74:77]
	ds_read_b128 v[130:133], v107 offset:16384
	ds_read_b128 v[134:137], v107 offset:18432
	s_waitcnt lgkmcnt(3)
	v_mfma_f32_16x16x32_f16 v[74:77], v[22:25], v[54:57], v[10:13]
	v_mfma_f32_16x16x32_f16 v[112:115], v[58:61], v[54:57], v[14:17]
	s_nop 1
	ds_read_b128 v[10:13], v103 offset:24576
	ds_read_b128 v[14:17], v103 offset:26624
	s_waitcnt lgkmcnt(1)
	v_mfma_f32_16x16x32_f16 v[46:49], v[130:133], v[10:13], v[46:49]
	v_mfma_f32_16x16x32_f16 v[38:41], v[134:137], v[10:13], v[38:41]
	s_waitcnt lgkmcnt(0)
	v_mfma_f32_16x16x32_f16 v[34:37], v[130:133], v[14:17], v[34:37]
	v_mfma_f32_16x16x32_f16 v[30:33], v[134:137], v[14:17], v[30:33]
	ds_read_b128 v[10:13], v103 offset:28672
	ds_read_b128 v[14:17], v103 offset:30720
	ds_read_b128 v[146:149], v103 offset:32768
	ds_read_b128 v[150:153], v103 offset:34816
	v_mfma_f32_16x16x32_f16 v[122:125], v[22:25], v[70:73], v[18:21]
	s_waitcnt lgkmcnt(3)
	v_mfma_f32_16x16x32_f16 v[42:45], v[130:133], v[10:13], v[42:45]
	v_mfma_f32_16x16x32_f16 v[50:53], v[134:137], v[10:13], v[50:53]
	s_waitcnt lgkmcnt(2)
	v_mfma_f32_16x16x32_f16 v[54:57], v[130:133], v[14:17], v[26:29]
	s_nop 2
	global_load_dwordx4 v[26:29], v[154:155], off offset:384
	global_load_dwordx4 v[22:25], v[156:157], off offset:384
	global_load_dwordx4 v[18:21], v[158:159], off offset:384
	global_load_dwordx4 v[10:13], v[160:161], off offset:384
	v_mfma_f32_16x16x32_f16 v[70:73], v[58:61], v[70:73], v[62:65]
	v_mfma_f32_16x16x32_f16 v[58:61], v[134:137], v[14:17], v[66:69]
	global_load_dwordx4 v[14:17], v[162:163], off offset:384
	s_waitcnt vmcnt(9)
	ds_write_b128 v1, v[126:129]
	s_waitcnt vmcnt(8)
	ds_write_b128 v1, v[108:111] offset:8192
	s_waitcnt vmcnt(7)
	ds_write_b128 v1, v[138:141] offset:16384
	s_waitcnt vmcnt(6)
	ds_write_b128 v1, v[118:121] offset:49152
	s_waitcnt vmcnt(5)
	ds_write_b128 v1, v[142:145] offset:57344
	s_waitcnt lgkmcnt(0)
	v_mfma_f32_16x16x32_f16 v[62:65], v[130:133], v[146:149], v[74:77]
	s_barrier
	v_mfma_f32_16x16x32_f16 v[66:69], v[134:137], v[146:149], v[112:115]
	v_mfma_f32_16x16x32_f16 v[74:77], v[130:133], v[150:153], v[122:125]
	v_mfma_f32_16x16x32_f16 v[70:73], v[134:137], v[150:153], v[70:73]
	s_cbranch_scc1 .LBB3_53
	ds_read_b128 v[94:97], v104 offset:49152
	ds_read_b128 v[98:101], v104 offset:51200
	ds_read_b128 v[108:111], v102
	ds_read_b128 v[112:115], v102 offset:2048
	v_add_u32_e32 v81, 0x10000, v1
	s_lshl_b64 s[0:1], s[0:1], 1
	s_add_u32 s0, s10, s0
	s_waitcnt lgkmcnt(1)
	v_mfma_f32_16x16x32_f16 v[46:49], v[94:97], v[108:111], v[46:49]
	s_addc_u32 s1, s11, s1
	v_cmp_gt_u32_e32 vcc, s18, v79
	v_mfma_f32_16x16x32_f16 v[38:41], v[98:101], v[108:111], v[38:41]
	s_waitcnt lgkmcnt(0)
	v_mfma_f32_16x16x32_f16 v[34:37], v[94:97], v[112:115], v[34:37]
	v_mfma_f32_16x16x32_f16 v[30:33], v[98:101], v[112:115], v[30:33]
	ds_read_b128 v[108:111], v102 offset:4096
	ds_read_b128 v[112:115], v102 offset:6144
	s_waitcnt lgkmcnt(1)
	v_mfma_f32_16x16x32_f16 v[42:45], v[94:97], v[108:111], v[42:45]
	v_mfma_f32_16x16x32_f16 v[50:53], v[98:101], v[108:111], v[50:53]
	s_waitcnt lgkmcnt(0)
	v_mfma_f32_16x16x32_f16 v[54:57], v[94:97], v[112:115], v[54:57]
	v_mfma_f32_16x16x32_f16 v[58:61], v[98:101], v[112:115], v[58:61]
	ds_read_b128 v[108:111], v102 offset:8192
	ds_read_b128 v[112:115], v102 offset:10240
	s_waitcnt lgkmcnt(1)
	v_mfma_f32_16x16x32_f16 v[62:65], v[94:97], v[108:111], v[62:65]
	s_waitcnt lgkmcnt(0)
	v_mfma_f32_16x16x32_f16 v[74:77], v[94:97], v[112:115], v[74:77]
	ds_read_b128 v[94:97], v105 offset:49152
	v_mfma_f32_16x16x32_f16 v[66:69], v[98:101], v[108:111], v[66:69]
	v_mfma_f32_16x16x32_f16 v[70:73], v[98:101], v[112:115], v[70:73]
	ds_read_b128 v[98:101], v105 offset:51200
	ds_read_b128 v[108:111], v103
	ds_read_b128 v[112:115], v103 offset:2048
	s_waitcnt lgkmcnt(1)
	v_mfma_f32_16x16x32_f16 v[46:49], v[94:97], v[108:111], v[46:49]
	v_mfma_f32_16x16x32_f16 v[38:41], v[98:101], v[108:111], v[38:41]
	s_waitcnt lgkmcnt(0)
	v_mfma_f32_16x16x32_f16 v[34:37], v[94:97], v[112:115], v[34:37]
	v_mfma_f32_16x16x32_f16 v[30:33], v[98:101], v[112:115], v[30:33]
	ds_read_b128 v[108:111], v103 offset:4096
	ds_read_b128 v[112:115], v103 offset:6144
	s_waitcnt lgkmcnt(1)
	v_mfma_f32_16x16x32_f16 v[42:45], v[94:97], v[108:111], v[42:45]
	v_mfma_f32_16x16x32_f16 v[50:53], v[98:101], v[108:111], v[50:53]
	s_waitcnt lgkmcnt(0)
	v_mfma_f32_16x16x32_f16 v[54:57], v[94:97], v[112:115], v[54:57]
	v_mfma_f32_16x16x32_f16 v[58:61], v[98:101], v[112:115], v[58:61]
	ds_read_b128 v[108:111], v103 offset:8192
	ds_read_b128 v[112:115], v103 offset:10240
	s_waitcnt vmcnt(4)
	ds_write_b128 v1, v[26:29] offset:24576
	s_waitcnt vmcnt(3)
	ds_write_b128 v1, v[22:25] offset:32768
	s_waitcnt vmcnt(2)
	ds_write_b128 v1, v[18:21] offset:40960
	s_waitcnt vmcnt(1)
	ds_write_b128 v81, v[10:13]
	s_waitcnt vmcnt(0)
	ds_write_b128 v81, v[14:17] offset:8192
	s_waitcnt lgkmcnt(0)
	s_barrier
	ds_read_b128 v[10:13], v106 offset:16384
	ds_read_b128 v[18:21], v106 offset:18432
	ds_read_b128 v[22:25], v102 offset:24576
	ds_read_b128 v[26:29], v102 offset:26624
	s_waitcnt lgkmcnt(1)
	v_mfma_f32_16x16x32_f16 v[46:49], v[10:13], v[22:25], v[46:49]
	v_mfma_f32_16x16x32_f16 v[22:25], v[18:21], v[22:25], v[38:41]
	s_waitcnt lgkmcnt(0)
	v_mfma_f32_16x16x32_f16 v[34:37], v[10:13], v[26:29], v[34:37]
	v_mfma_f32_16x16x32_f16 v[26:29], v[18:21], v[26:29], v[30:33]
	s_nop 2
	ds_read_b128 v[30:33], v102 offset:28672
	ds_read_b128 v[38:41], v102 offset:30720
	v_mfma_f32_16x16x32_f16 v[62:65], v[94:97], v[108:111], v[62:65]
	v_mfma_f32_16x16x32_f16 v[74:77], v[94:97], v[112:115], v[74:77]
	v_mfma_f32_16x16x32_f16 v[14:17], v[98:101], v[112:115], v[70:73]
	s_waitcnt lgkmcnt(1)
	v_mfma_f32_16x16x32_f16 v[70:73], v[10:13], v[30:33], v[42:45]
	s_waitcnt lgkmcnt(0)
	v_mfma_f32_16x16x32_f16 v[94:97], v[10:13], v[38:41], v[54:57]
	v_mfma_f32_16x16x32_f16 v[58:61], v[18:21], v[38:41], v[58:61]
	ds_read_b128 v[38:41], v102 offset:32768
	ds_read_b128 v[42:45], v102 offset:34816
	v_mfma_f32_16x16x32_f16 v[66:69], v[98:101], v[108:111], v[66:69]
	s_waitcnt lgkmcnt(1)
	v_mfma_f32_16x16x32_f16 v[62:65], v[10:13], v[38:41], v[62:65]
	s_waitcnt lgkmcnt(0)
	v_mfma_f32_16x16x32_f16 v[10:13], v[10:13], v[42:45], v[74:77]
	s_nop 2
	ds_read_b128 v[74:77], v107 offset:16384
	v_mfma_f32_16x16x32_f16 v[30:33], v[18:21], v[30:33], v[50:53]
	v_mfma_f32_16x16x32_f16 v[66:69], v[18:21], v[38:41], v[66:69]
	v_mfma_f32_16x16x32_f16 v[98:101], v[18:21], v[42:45], v[14:17]
	ds_read_b128 v[104:107], v107 offset:18432
	s_nop 1
	ds_read_b128 v[14:17], v103 offset:24576
	ds_read_b128 v[18:21], v103 offset:26624
	s_waitcnt lgkmcnt(1)
	v_mfma_f32_16x16x32_f16 v[54:57], v[74:77], v[14:17], v[46:49]
	v_mfma_f32_16x16x32_f16 v[50:53], v[104:107], v[14:17], v[22:25]
	s_waitcnt lgkmcnt(0)
	v_mfma_f32_16x16x32_f16 v[46:49], v[74:77], v[18:21], v[34:37]
	v_mfma_f32_16x16x32_f16 v[42:45], v[104:107], v[18:21], v[26:29]
	ds_read_b128 v[14:17], v103 offset:28672
	ds_read_b128 v[18:21], v103 offset:30720
	s_waitcnt lgkmcnt(1)
	v_mfma_f32_16x16x32_f16 v[38:41], v[74:77], v[14:17], v[70:73]
	v_mfma_f32_16x16x32_f16 v[34:37], v[104:107], v[14:17], v[30:33]
	s_waitcnt lgkmcnt(0)
	v_mfma_f32_16x16x32_f16 v[26:29], v[104:107], v[18:21], v[58:61]
	ds_read_b128 v[14:17], v103 offset:32768
	s_nop 1
	ds_read_b128 v[58:61], v103 offset:34816
	s_waitcnt lgkmcnt(1)
	v_mfma_f32_16x16x32_f16 v[22:25], v[74:77], v[14:17], v[62:65]
	s_nop 2
	v_lshlrev_b32_e32 v62, 1, v92
	v_mov_b32_e32 v63, 0
	v_mfma_f32_16x16x32_f16 v[30:33], v[74:77], v[18:21], v[94:97]
	v_mfma_f32_16x16x32_f16 v[18:21], v[104:107], v[14:17], v[66:69]
	s_waitcnt lgkmcnt(0)
	v_mfma_f32_16x16x32_f16 v[14:17], v[74:77], v[58:61], v[10:13]
	s_nop 2
	v_lshl_add_u64 v[10:11], s[0:1], 0, v[62:63]
	v_lshlrev_b32_e32 v62, 1, v0
	v_lshl_add_u64 v[0:1], v[10:11], 0, v[62:63]
	v_mfma_f32_16x16x32_f16 v[10:13], v[104:107], v[58:61], v[98:101]
	v_mbcnt_lo_u32_b32 v196, -1, 0
	v_mbcnt_hi_u32_b32 v196, -1, v196
	v_and_b32_e32 v197, 15, v196
	v_lshrrev_b32_e32 v198, 4, v196
	v_lshrrev_b32_e32 v222, 10, v81
	s_nop 0
	v_readfirstlane_b32 s36, v222
	s_nop 3
	s_and_b32 s36, s36, 7
	s_mulk_i32 s36, 0x500
	v_mul_u32_u24_e32 v199, 0x50, v197
	v_lshl_add_u32 v199, v198, 3, v199
	v_add_u32_e32 v199, s36, v199
	v_lshrrev_b32_e32 v200, 2, v196
	v_and_b32_e32 v201, 3, v196
	v_mul_u32_u24_e32 v202, 0x50, v200
	v_lshl_add_u32 v202, v201, 4, v202
	v_add_u32_e32 v202, s36, v202
	v_lshlrev_b32_e32 v203, 2, v200
	v_add_u32_e32 v204, 32, v203
	v_lshlrev_b32_e32 v220, 4, v201
	v_mov_b32_e32 v221, 0
	v_sub_u32_e32 v205, v79, v197
	v_add_u32_e32 v205, v205, v200
	s_mov_b64 s[0:1], exec
	s_cbranch_execz .LBB3_56
	v_add_f32_e32 v55, v7, v55
	v_ashrrev_i32_e32 v91, 31, v90
	v_add_f32_e32 v54, v6, v54
	v_max_f32_e32 v60, 0, v55
	v_add_f32_e32 v55, v8, v56
	v_add_f32_e32 v56, v9, v57
	v_lshlrev_b64 v[58:59], 11, v[90:91]
	v_max_f32_e32 v54, 0, v54
	v_max_f32_e32 v55, 0, v55
	v_max_f32_e32 v56, 0, v56
	v_lshl_add_u64 v[58:59], v[0:1], 0, v[58:59]
	v_cvt_pk_f16_f32 v55, v55, v56
	v_cvt_pk_f16_f32 v54, v54, v60
	v_add_f32_e32 v51, v3, v51
	ds_write_b64 v199, v[54:55]
	v_add_f32_e32 v50, v2, v50
	v_max_f32_e32 v54, 0, v51
	v_add_f32_e32 v51, v4, v52
	v_add_f32_e32 v52, v5, v53
	v_max_f32_e32 v50, 0, v50
	v_max_f32_e32 v51, 0, v51
	v_max_f32_e32 v52, 0, v52
	v_cvt_pk_f16_f32 v51, v51, v52
	v_cvt_pk_f16_f32 v50, v50, v54
	ds_write_b64 v199, v[50:51] offset:32
	s_waitcnt lgkmcnt(0)
	ds_read_b128 v[208:211], v202
	ds_bpermute_b32 v216, v203, v58
	ds_bpermute_b32 v217, v203, v59
	v_add_u32_e32 v222, 0, v205
	v_cmp_gt_u32_e64 s[38:39], s18, v222
	s_waitcnt lgkmcnt(0)
	v_lshl_add_u64 v[216:217], v[216:217], 0, v[220:221]
	s_mov_b64 s[42:43], exec
	s_and_b64 exec, s[42:43], s[38:39]
	global_store_dwordx4 v[216:217], v[208:211], off
	s_mov_b64 exec, s[42:43]
.LBB3_56:
	s_or_b64 exec, exec, s[0:1]
	v_or_b32_e32 v50, 16, v79
	v_cmp_gt_u32_e32 vcc, s18, v50
	s_mov_b64 s[0:1], exec
	s_cbranch_execz .LBB3_58
	v_add_f32_e32 v47, v7, v47
	v_ashrrev_i32_e32 v89, 31, v88
	v_add_f32_e32 v46, v6, v46
	v_max_f32_e32 v52, 0, v47
	v_add_f32_e32 v47, v8, v48
	v_add_f32_e32 v48, v9, v49
	v_lshlrev_b64 v[50:51], 11, v[88:89]
	v_max_f32_e32 v46, 0, v46
	v_max_f32_e32 v47, 0, v47
	v_max_f32_e32 v48, 0, v48
	v_lshl_add_u64 v[50:51], v[0:1], 0, v[50:51]
	v_cvt_pk_f16_f32 v47, v47, v48
	v_cvt_pk_f16_f32 v46, v46, v52
	v_add_f32_e32 v43, v3, v43
	ds_write_b64 v199, v[46:47]
	v_add_f32_e32 v42, v2, v42
	v_max_f32_e32 v46, 0, v43
	v_add_f32_e32 v43, v4, v44
	v_add_f32_e32 v44, v5, v45
	v_max_f32_e32 v42, 0, v42
	v_max_f32_e32 v43, 0, v43
	v_max_f32_e32 v44, 0, v44
	v_cvt_pk_f16_f32 v43, v43, v44
	v_cvt_pk_f16_f32 v42, v42, v46
	ds_write_b64 v199, v[42:43] offset:32
	s_waitcnt lgkmcnt(0)
	ds_read_b128 v[208:211], v202
	ds_bpermute_b32 v216, v203, v50
	ds_bpermute_b32 v217, v203, v51
	v_add_u32_e32 v222, 16, v205
	v_cmp_gt_u32_e64 s[38:39], s18, v222
	s_waitcnt lgkmcnt(0)
	v_lshl_add_u64 v[216:217], v[216:217], 0, v[220:221]
	s_mov_b64 s[42:43], exec
	s_and_b64 exec, s[42:43], s[38:39]
	global_store_dwordx4 v[216:217], v[208:211], off
	s_mov_b64 exec, s[42:43]
.LBB3_58:
	s_or_b64 exec, exec, s[0:1]
	v_add_u32_e32 v42, 32, v79
	v_cmp_gt_u32_e32 vcc, s18, v42
	s_mov_b64 s[0:1], exec
	s_cbranch_execz .LBB3_60
	v_add_f32_e32 v39, v7, v39
	v_ashrrev_i32_e32 v87, 31, v86
	v_add_f32_e32 v38, v6, v38
	v_max_f32_e32 v44, 0, v39
	v_add_f32_e32 v39, v8, v40
	v_add_f32_e32 v40, v9, v41
	v_lshlrev_b64 v[42:43], 11, v[86:87]
	v_max_f32_e32 v38, 0, v38
	v_max_f32_e32 v39, 0, v39
	v_max_f32_e32 v40, 0, v40
	v_lshl_add_u64 v[42:43], v[0:1], 0, v[42:43]
	v_cvt_pk_f16_f32 v39, v39, v40
	v_cvt_pk_f16_f32 v38, v38, v44
	v_add_f32_e32 v35, v3, v35
	ds_write_b64 v199, v[38:39]
	v_add_f32_e32 v34, v2, v34
	v_max_f32_e32 v38, 0, v35
	v_add_f32_e32 v35, v4, v36
	v_add_f32_e32 v36, v5, v37
	v_max_f32_e32 v34, 0, v34
	v_max_f32_e32 v35, 0, v35
	v_max_f32_e32 v36, 0, v36
	v_cvt_pk_f16_f32 v35, v35, v36
	v_cvt_pk_f16_f32 v34, v34, v38
	ds_write_b64 v199, v[34:35] offset:32
	s_waitcnt lgkmcnt(0)
	ds_read_b128 v[208:211], v202
	ds_bpermute_b32 v216, v203, v42
	ds_bpermute_b32 v217, v203, v43
	v_add_u32_e32 v222, 32, v205
	v_cmp_gt_u32_e64 s[38:39], s18, v222
	s_waitcnt lgkmcnt(0)
	v_lshl_add_u64 v[216:217], v[216:217], 0, v[220:221]
	s_mov_b64 s[42:43], exec
	s_and_b64 exec, s[42:43], s[38:39]
	global_store_dwordx4 v[216:217], v[208:211], off
	s_mov_b64 exec, s[42:43]
.LBB3_60:
	s_or_b64 exec, exec, s[0:1]
	v_add_u32_e32 v34, 48, v79
	v_cmp_gt_u32_e32 vcc, s18, v34
	s_mov_b64 s[0:1], exec
	s_cbranch_execz .LBB3_62
	v_add_f32_e32 v31, v7, v31
	v_ashrrev_i32_e32 v83, 31, v82
	v_add_f32_e32 v30, v6, v30
	v_max_f32_e32 v36, 0, v31
	v_add_f32_e32 v31, v8, v32
	v_add_f32_e32 v32, v9, v33
	v_lshlrev_b64 v[34:35], 11, v[82:83]
	v_max_f32_e32 v30, 0, v30
	v_max_f32_e32 v31, 0, v31
	v_max_f32_e32 v32, 0, v32
	v_lshl_add_u64 v[34:35], v[0:1], 0, v[34:35]
	v_cvt_pk_f16_f32 v31, v31, v32
	v_cvt_pk_f16_f32 v30, v30, v36
	v_add_f32_e32 v27, v3, v27
	ds_write_b64 v199, v[30:31]
	v_add_f32_e32 v26, v2, v26
	v_max_f32_e32 v30, 0, v27
	v_add_f32_e32 v27, v4, v28
	v_add_f32_e32 v28, v5, v29
	v_max_f32_e32 v26, 0, v26
	v_max_f32_e32 v27, 0, v27
	v_max_f32_e32 v28, 0, v28
	v_cvt_pk_f16_f32 v27, v27, v28
	v_cvt_pk_f16_f32 v26, v26, v30
	ds_write_b64 v199, v[26:27] offset:32
	s_waitcnt lgkmcnt(0)
	ds_read_b128 v[208:211], v202
	ds_bpermute_b32 v216, v203, v34
	ds_bpermute_b32 v217, v203, v35
	v_add_u32_e32 v222, 48, v205
	v_cmp_gt_u32_e64 s[38:39], s18, v222
	s_waitcnt lgkmcnt(0)
	v_lshl_add_u64 v[216:217], v[216:217], 0, v[220:221]
	s_mov_b64 s[42:43], exec
	s_and_b64 exec, s[42:43], s[38:39]
	global_store_dwordx4 v[216:217], v[208:211], off
	s_mov_b64 exec, s[42:43]
.LBB3_62:
	s_or_b64 exec, exec, s[0:1]
	v_add_u32_e32 v26, 64, v79
	v_cmp_gt_u32_e32 vcc, s18, v26
	s_mov_b64 s[0:1], exec
	s_cbranch_execz .LBB3_64
	v_add_f32_e32 v23, v7, v23
	v_ashrrev_i32_e32 v81, 31, v80
	v_add_f32_e32 v22, v6, v22
	v_max_f32_e32 v28, 0, v23
	v_add_f32_e32 v23, v8, v24
	v_add_f32_e32 v24, v9, v25
	v_lshlrev_b64 v[26:27], 11, v[80:81]
	v_max_f32_e32 v22, 0, v22
	v_max_f32_e32 v23, 0, v23
	v_max_f32_e32 v24, 0, v24
	v_lshl_add_u64 v[26:27], v[0:1], 0, v[26:27]
	v_cvt_pk_f16_f32 v23, v23, v24
	v_cvt_pk_f16_f32 v22, v22, v28
	v_add_f32_e32 v19, v3, v19
	ds_write_b64 v199, v[22:23]
	v_add_f32_e32 v18, v2, v18
	v_max_f32_e32 v22, 0, v19
	v_add_f32_e32 v19, v4, v20
	v_add_f32_e32 v20, v5, v21
	v_max_f32_e32 v18, 0, v18
	v_max_f32_e32 v19, 0, v19
	v_max_f32_e32 v20, 0, v20
	v_cvt_pk_f16_f32 v19, v19, v20
	v_cvt_pk_f16_f32 v18, v18, v22
	ds_write_b64 v199, v[18:19] offset:32
	s_waitcnt lgkmcnt(0)
	ds_read_b128 v[208:211], v202
	ds_bpermute_b32 v216, v203, v26
	ds_bpermute_b32 v217, v203, v27
	v_add_u32_e32 v222, 64, v205
	v_cmp_gt_u32_e64 s[38:39], s18, v222
	s_waitcnt lgkmcnt(0)
	v_lshl_add_u64 v[216:217], v[216:217], 0, v[220:221]
	s_mov_b64 s[42:43], exec
	s_and_b64 exec, s[42:43], s[38:39]
	global_store_dwordx4 v[216:217], v[208:211], off
	s_mov_b64 exec, s[42:43]
.LBB3_64:
	s_or_b64 exec, exec, s[0:1]
	v_add_u32_e32 v18, 0x50, v79
	v_cmp_gt_u32_e32 vcc, s18, v18
	s_mov_b64 s[0:1], exec
	s_cbranch_execz .LBB3_66
	v_add_f32_e32 v7, v7, v15
	v_ashrrev_i32_e32 v79, 31, v78
	v_add_f32_e32 v6, v6, v14
	v_max_f32_e32 v14, 0, v7
	v_add_f32_e32 v7, v8, v16
	v_add_f32_e32 v8, v9, v17
	v_lshlrev_b64 v[18:19], 11, v[78:79]
	v_max_f32_e32 v6, 0, v6
	v_max_f32_e32 v7, 0, v7
	v_max_f32_e32 v8, 0, v8
	v_lshl_add_u64 v[0:1], v[0:1], 0, v[18:19]
	v_cvt_pk_f16_f32 v7, v7, v8
	v_cvt_pk_f16_f32 v6, v6, v14
	v_add_f32_e32 v3, v3, v11
	ds_write_b64 v199, v[6:7]
	v_add_f32_e32 v2, v2, v10
	v_max_f32_e32 v6, 0, v3
	v_add_f32_e32 v3, v4, v12
	v_add_f32_e32 v4, v5, v13
	v_max_f32_e32 v2, 0, v2
	v_max_f32_e32 v3, 0, v3
	v_max_f32_e32 v4, 0, v4
	v_cvt_pk_f16_f32 v3, v3, v4
	v_cvt_pk_f16_f32 v2, v2, v6
	ds_write_b64 v199, v[2:3] offset:32
	s_waitcnt lgkmcnt(0)
	ds_read_b128 v[208:211], v202
	ds_bpermute_b32 v216, v203, v0
	ds_bpermute_b32 v217, v203, v1
	v_add_u32_e32 v222, 80, v205
	v_cmp_gt_u32_e64 s[38:39], s18, v222
	s_waitcnt lgkmcnt(0)
	v_lshl_add_u64 v[216:217], v[216:217], 0, v[220:221]
	s_mov_b64 s[42:43], exec
	s_and_b64 exec, s[42:43], s[38:39]
	global_store_dwordx4 v[216:217], v[208:211], off
	s_mov_b64 exec, s[42:43]

	.amdhsa_kernel _Z11gemm_kernelILi0ELi192ELi256ELi128ELi2ELi4ELi2ELi2ELi64EEvPKDF16_PDF16_PKiS4_S1_S1_PKf
		.amdhsa_group_segment_fixed_size 0
		.amdhsa_private_segment_fixed_size 0
		.amdhsa_kernarg_size 56
		.amdhsa_user_sgpr_count 2
		.amdhsa_user_sgpr_dispatch_ptr 0
		.amdhsa_user_sgpr_queue_ptr 0
		.amdhsa_user_sgpr_kernarg_segment_ptr 1
		.amdhsa_user_sgpr_dispatch_id 0
		.amdhsa_user_sgpr_kernarg_preload_length 0
		.amdhsa_user_sgpr_kernarg_preload_offset 0
		.amdhsa_user_sgpr_private_segment_size 0
		.amdhsa_uses_dynamic_stack 0
		.amdhsa_enable_private_segment 0
		.amdhsa_system_sgpr_workgroup_id_x 1
		.amdhsa_system_sgpr_workgroup_id_y 0
		.amdhsa_system_sgpr_workgroup_id_z 0
		.amdhsa_system_sgpr_workgroup_info 0
		.amdhsa_system_vgpr_workitem_id 0
		.amdhsa_next_free_vgpr 254
		.amdhsa_next_free_sgpr 44
		.amdhsa_accum_offset 256
		.amdhsa_reserve_vcc 1
		.amdhsa_float_round_mode_32 0
		.amdhsa_float_round_mode_16_64 0
		.amdhsa_float_denorm_mode_32 3
		.amdhsa_float_denorm_mode_16_64 3
		.amdhsa_dx10_clamp 1
		.amdhsa_ieee_mode 1
		.amdhsa_fp16_overflow 0
		.amdhsa_tg_split 0
		.amdhsa_exception_fp_ieee_invalid_op 0
		.amdhsa_exception_fp_denorm_src 0
		.amdhsa_exception_fp_ieee_div_zero 0
		.amdhsa_exception_fp_ieee_overflow 0
		.amdhsa_exception_fp_ieee_underflow 0
		.amdhsa_exception_fp_ieee_inexact 0
		.amdhsa_exception_int_div_zero 0
	.end_amdhsa_kernel

_Z11gemm_kernelILi0ELi96ELi256ELi128ELi2ELi4ELi2ELi2ELi64EEvPKDF16_PDF16_PKiS4_S1_S1_PKf:
	s_load_dwordx2 s[4:5], s[0:1], 0x18
	s_waitcnt lgkmcnt(0)
	s_load_dword s3, s[4:5], 0x7fc
	s_waitcnt lgkmcnt(0)
	s_lshl_b32 s6, s3, 3
	s_add_i32 s6, s6, 56
	s_andn2_b32 s6, s6, 63
	s_cmp_ge_i32 s2, s6
	s_cbranch_scc0 .LBB4_2
	s_sub_i32 s6, s2, s6
	s_lshr_b32 s6, s6, 2
	s_and_b32 s7, s2, 7
	s_and_b32 s6, s6, 0x3ffffff8
	s_add_i32 s7, s3, s7
	s_bfe_u32 s25, s2, 0x20003
	s_add_i32 s6, s7, s6
	s_mov_b64 s[8:9], -1
	s_cbranch_execz .LBB4_3
	s_branch .LBB4_4

.LBB4_37:
	s_or_b64 exec, exec, s[6:7]
	s_waitcnt vmcnt(3)
	ds_write_b128 v154, v[42:45]
	s_waitcnt vmcnt(2)
	ds_write_b128 v154, v[46:49] offset:8192
	s_waitcnt vmcnt(1)
	ds_write_b128 v154, v[50:53] offset:16384
	s_waitcnt vmcnt(0)
	ds_write_b128 v154, v[54:57] offset:24576
	s_waitcnt lgkmcnt(0)
	s_barrier
	ds_read_b128 v[26:29], v162 offset:57344
	ds_read_b128 v[34:37], v161 offset:12288
	ds_read_b128 v[42:45], v162 offset:59392
	ds_read_b128 v[46:49], v161 offset:14336
	ds_read_b128 v[54:57], v162 offset:61440
	s_waitcnt lgkmcnt(3)
	v_mfma_f32_16x16x32_f16 v[50:53], v[26:29], v[34:37], v[78:81]
	s_lshl_b64 s[2:3], s[16:17], 1
	s_add_u32 s2, s10, s2
	s_addc_u32 s3, s11, s3
	s_waitcnt lgkmcnt(2)
	v_mfma_f32_16x16x32_f16 v[78:81], v[42:45], v[34:37], v[82:85]
	v_cmp_gt_u32_e32 vcc, s24, v133
	s_waitcnt lgkmcnt(0)
	v_mfma_f32_16x16x32_f16 v[82:85], v[54:57], v[34:37], v[86:89]
	s_nop 2
	ds_read_b128 v[86:89], v162 offset:63488
	ds_read_b128 v[90:93], v160 offset:12288
	ds_read_b128 v[98:101], v163 offset:59392
	ds_read_b128 v[102:105], v163 offset:61440
	s_waitcnt lgkmcnt(3)
	v_mfma_f32_16x16x32_f16 v[22:25], v[86:89], v[34:37], v[22:25]
	v_mfma_f32_16x16x32_f16 v[34:37], v[26:29], v[46:49], v[58:61]
	v_mfma_f32_16x16x32_f16 v[94:97], v[42:45], v[46:49], v[62:65]
	v_mfma_f32_16x16x32_f16 v[66:69], v[54:57], v[46:49], v[66:69]
	v_mfma_f32_16x16x32_f16 v[70:73], v[86:89], v[46:49], v[70:73]
	ds_read_b128 v[46:49], v161 offset:16384
	s_waitcnt lgkmcnt(0)
	v_mfma_f32_16x16x32_f16 v[26:29], v[26:29], v[46:49], v[30:33]
	s_nop 2
	ds_read_b128 v[30:33], v163 offset:57344
	v_mfma_f32_16x16x32_f16 v[58:61], v[98:101], v[90:93], v[78:81]
	s_nop 2
	ds_read_b128 v[78:81], v163 offset:63488
	v_mfma_f32_16x16x32_f16 v[18:21], v[54:57], v[46:49], v[18:21]
	s_waitcnt lgkmcnt(1)
	v_mfma_f32_16x16x32_f16 v[62:65], v[30:33], v[90:93], v[50:53]
	v_mfma_f32_16x16x32_f16 v[54:57], v[102:105], v[90:93], v[82:85]
	s_waitcnt lgkmcnt(0)
	v_mfma_f32_16x16x32_f16 v[50:53], v[78:81], v[90:93], v[22:25]
	s_nop 2
	ds_read_b128 v[22:25], v160 offset:14336
	ds_read_b128 v[82:85], v160 offset:16384
	v_mfma_f32_16x16x32_f16 v[74:77], v[42:45], v[46:49], v[74:77]
	v_mfma_f32_16x16x32_f16 v[86:89], v[86:89], v[46:49], v[38:41]
	s_waitcnt lgkmcnt(1)
	v_mfma_f32_16x16x32_f16 v[38:41], v[102:105], v[22:25], v[66:69]
	s_nop 2
	v_lshlrev_b32_e32 v66, 1, v135
	v_mov_b32_e32 v67, 0
	v_mfma_f32_16x16x32_f16 v[46:49], v[30:33], v[22:25], v[34:37]
	v_mfma_f32_16x16x32_f16 v[42:45], v[98:101], v[22:25], v[94:97]
	v_mfma_f32_16x16x32_f16 v[34:37], v[78:81], v[22:25], v[70:73]
	s_waitcnt lgkmcnt(0)
	v_mfma_f32_16x16x32_f16 v[22:25], v[102:105], v[82:85], v[18:21]
	s_nop 2
	v_lshl_add_u64 v[18:19], s[2:3], 0, v[66:67]
	v_lshlrev_b32_e32 v66, 1, v131
	v_mfma_f32_16x16x32_f16 v[30:33], v[30:33], v[82:85], v[26:29]
	v_lshl_add_u64 v[66:67], v[18:19], 0, v[66:67]
	v_mfma_f32_16x16x32_f16 v[26:29], v[98:101], v[82:85], v[74:77]
	v_mfma_f32_16x16x32_f16 v[18:21], v[78:81], v[82:85], v[86:89]
	v_mbcnt_lo_u32_b32 v196, -1, 0
	v_mbcnt_hi_u32_b32 v196, -1, v196
	v_and_b32_e32 v197, 15, v196
	v_lshrrev_b32_e32 v198, 4, v196
	v_lshrrev_b32_e32 v222, 10, v137
	s_nop 0
	v_readfirstlane_b32 s36, v222
	s_nop 3
	s_and_b32 s36, s36, 7
	s_mulk_i32 s36, 0x900
	s_add_u32 s36, s36, 0x6000
	v_mul_u32_u24_e32 v199, 0x90, v197
	v_lshl_add_u32 v199, v198, 3, v199
	v_add_u32_e32 v199, s36, v199
	v_lshrrev_b32_e32 v200, 3, v196
	v_and_b32_e32 v201, 7, v196
	v_mul_u32_u24_e32 v202, 0x90, v200
	v_lshl_add_u32 v202, v201, 4, v202
	v_add_u32_e32 v202, s36, v202
	v_lshlrev_b32_e32 v203, 2, v200
	v_add_u32_e32 v204, 32, v203
	v_lshlrev_b32_e32 v220, 4, v201
	v_mov_b32_e32 v221, 0
	v_sub_u32_e32 v205, v133, v197
	v_add_u32_e32 v205, v205, v200
	s_mov_b64 s[2:3], exec
	s_cbranch_execz .LBB4_39
	v_add_f32_e32 v63, v15, v63
	v_ashrrev_i32_e32 v137, 31, v136
	v_add_f32_e32 v62, v14, v62
	v_max_f32_e32 v70, 0, v63
	v_add_f32_e32 v63, v16, v64
	v_add_f32_e32 v64, v17, v65
	v_lshlrev_b64 v[68:69], 11, v[136:137]
	v_max_f32_e32 v62, 0, v62
	v_max_f32_e32 v63, 0, v63
	v_max_f32_e32 v64, 0, v64
	v_lshl_add_u64 v[68:69], v[66:67], 0, v[68:69]
	v_cvt_pk_f16_f32 v63, v63, v64
	v_cvt_pk_f16_f32 v62, v62, v70
	v_add_f32_e32 v59, v11, v59
	ds_write_b64 v199, v[62:63]
	v_add_f32_e32 v58, v10, v58
	v_max_f32_e32 v62, 0, v59
	v_add_f32_e32 v59, v12, v60
	v_add_f32_e32 v60, v13, v61
	v_max_f32_e32 v58, 0, v58
	v_max_f32_e32 v59, 0, v59
	v_max_f32_e32 v60, 0, v60
	v_cvt_pk_f16_f32 v59, v59, v60
	v_cvt_pk_f16_f32 v58, v58, v62
	v_add_f32_e32 v55, v7, v55
	ds_write_b64 v199, v[58:59] offset:32
	v_add_f32_e32 v54, v6, v54
	v_max_f32_e32 v58, 0, v55
	v_add_f32_e32 v55, v8, v56
	v_add_f32_e32 v56, v9, v57
	v_max_f32_e32 v54, 0, v54
	v_max_f32_e32 v55, 0, v55
	v_max_f32_e32 v56, 0, v56
	v_cvt_pk_f16_f32 v55, v55, v56
	v_cvt_pk_f16_f32 v54, v54, v58
	v_add_f32_e32 v51, v3, v51
	ds_write_b64 v199, v[54:55] offset:64
	v_add_f32_e32 v50, v2, v50
	v_max_f32_e32 v54, 0, v51
	v_add_f32_e32 v51, v4, v52
	v_add_f32_e32 v52, v5, v53
	v_max_f32_e32 v50, 0, v50
	v_max_f32_e32 v51, 0, v51
	v_max_f32_e32 v52, 0, v52
	v_cvt_pk_f16_f32 v51, v51, v52
	v_cvt_pk_f16_f32 v50, v50, v54
	ds_write_b64 v199, v[50:51] offset:96
	s_waitcnt lgkmcnt(0)
	ds_read_b128 v[208:211], v202
	ds_read_b128 v[212:215], v202 offset:1152
	ds_bpermute_b32 v216, v203, v68
	ds_bpermute_b32 v217, v203, v69
	ds_bpermute_b32 v218, v204, v68
	ds_bpermute_b32 v219, v204, v69
	v_add_u32_e32 v222, 0, v205
	v_cmp_gt_u32_e64 s[38:39], s24, v222
	v_add_u32_e32 v222, 8, v222
	v_cmp_gt_u32_e64 s[40:41], s24, v222
	s_waitcnt lgkmcnt(0)
	v_lshl_add_u64 v[216:217], v[216:217], 0, v[220:221]
	v_lshl_add_u64 v[218:219], v[218:219], 0, v[220:221]
	s_mov_b64 s[42:43], exec
	s_and_b64 exec, s[42:43], s[38:39]
	global_store_dwordx4 v[216:217], v[208:211], off
	s_and_b64 exec, s[42:43], s[40:41]
	global_store_dwordx4 v[218:219], v[212:215], off
	s_mov_b64 exec, s[42:43]
.LBB4_39:
	s_or_b64 exec, exec, s[2:3]
	v_add_u32_e32 v50, 16, v133
	v_cmp_gt_u32_e32 vcc, s24, v50
	s_mov_b64 s[2:3], exec
	s_cbranch_execz .LBB4_41
	v_add_f32_e32 v47, v15, v47
	v_ashrrev_i32_e32 v135, 31, v134
	v_add_f32_e32 v46, v14, v46
	v_max_f32_e32 v52, 0, v47
	v_add_f32_e32 v47, v16, v48
	v_add_f32_e32 v48, v17, v49
	v_lshlrev_b64 v[50:51], 11, v[134:135]
	v_max_f32_e32 v46, 0, v46
	v_max_f32_e32 v47, 0, v47
	v_max_f32_e32 v48, 0, v48
	v_lshl_add_u64 v[50:51], v[66:67], 0, v[50:51]
	v_cvt_pk_f16_f32 v47, v47, v48
	v_cvt_pk_f16_f32 v46, v46, v52
	v_add_f32_e32 v43, v11, v43
	ds_write_b64 v199, v[46:47]
	v_add_f32_e32 v42, v10, v42
	v_max_f32_e32 v46, 0, v43
	v_add_f32_e32 v43, v12, v44
	v_add_f32_e32 v44, v13, v45
	v_max_f32_e32 v42, 0, v42
	v_max_f32_e32 v43, 0, v43
	v_max_f32_e32 v44, 0, v44
	v_cvt_pk_f16_f32 v43, v43, v44
	v_cvt_pk_f16_f32 v42, v42, v46
	v_add_f32_e32 v39, v7, v39
	ds_write_b64 v199, v[42:43] offset:32
	v_add_f32_e32 v38, v6, v38
	v_max_f32_e32 v42, 0, v39
	v_add_f32_e32 v39, v8, v40
	v_add_f32_e32 v40, v9, v41
	v_max_f32_e32 v38, 0, v38
	v_max_f32_e32 v39, 0, v39
	v_max_f32_e32 v40, 0, v40
	v_cvt_pk_f16_f32 v39, v39, v40
	v_cvt_pk_f16_f32 v38, v38, v42
	v_add_f32_e32 v35, v3, v35
	ds_write_b64 v199, v[38:39] offset:64
	v_add_f32_e32 v34, v2, v34
	v_max_f32_e32 v38, 0, v35
	v_add_f32_e32 v35, v4, v36
	v_add_f32_e32 v36, v5, v37
	v_max_f32_e32 v34, 0, v34
	v_max_f32_e32 v35, 0, v35
	v_max_f32_e32 v36, 0, v36
	v_cvt_pk_f16_f32 v35, v35, v36
	v_cvt_pk_f16_f32 v34, v34, v38
	ds_write_b64 v199, v[34:35] offset:96
	s_waitcnt lgkmcnt(0)
	ds_read_b128 v[208:211], v202
	ds_read_b128 v[212:215], v202 offset:1152
	ds_bpermute_b32 v216, v203, v50
	ds_bpermute_b32 v217, v203, v51
	ds_bpermute_b32 v218, v204, v50
	ds_bpermute_b32 v219, v204, v51
	v_add_u32_e32 v222, 16, v205
	v_cmp_gt_u32_e64 s[38:39], s24, v222
	v_add_u32_e32 v222, 8, v222
	v_cmp_gt_u32_e64 s[40:41], s24, v222
	s_waitcnt lgkmcnt(0)
	v_lshl_add_u64 v[216:217], v[216:217], 0, v[220:221]
	v_lshl_add_u64 v[218:219], v[218:219], 0, v[220:221]
	s_mov_b64 s[42:43], exec
	s_and_b64 exec, s[42:43], s[38:39]
	global_store_dwordx4 v[216:217], v[208:211], off
	s_and_b64 exec, s[42:43], s[40:41]
	global_store_dwordx4 v[218:219], v[212:215], off
	s_mov_b64 exec, s[42:43]
.LBB4_41:
	s_or_b64 exec, exec, s[2:3]
	v_add_u32_e32 v34, 32, v133
	v_cmp_gt_u32_e32 vcc, s24, v34
	s_mov_b64 s[2:3], exec
	s_cbranch_execz .LBB4_43
	v_add_f32_e32 v15, v15, v31
	v_ashrrev_i32_e32 v133, 31, v132
	v_add_f32_e32 v14, v14, v30
	v_max_f32_e32 v30, 0, v15
	v_add_f32_e32 v15, v16, v32
	v_add_f32_e32 v16, v17, v33
	v_lshlrev_b64 v[34:35], 11, v[132:133]
	v_max_f32_e32 v14, 0, v14
	v_max_f32_e32 v15, 0, v15
	v_max_f32_e32 v16, 0, v16
	v_lshl_add_u64 v[34:35], v[66:67], 0, v[34:35]
	v_cvt_pk_f16_f32 v15, v15, v16
	v_cvt_pk_f16_f32 v14, v14, v30
	v_add_f32_e32 v11, v11, v27
	ds_write_b64 v199, v[14:15]
	v_add_f32_e32 v10, v10, v26
	v_max_f32_e32 v14, 0, v11
	v_add_f32_e32 v11, v12, v28
	v_add_f32_e32 v12, v13, v29
	v_max_f32_e32 v10, 0, v10
	v_max_f32_e32 v11, 0, v11
	v_max_f32_e32 v12, 0, v12
	v_cvt_pk_f16_f32 v11, v11, v12
	v_cvt_pk_f16_f32 v10, v10, v14
	v_add_f32_e32 v7, v7, v23
	ds_write_b64 v199, v[10:11] offset:32
	v_add_f32_e32 v6, v6, v22
	v_max_f32_e32 v10, 0, v7
	v_add_f32_e32 v7, v8, v24
	v_add_f32_e32 v8, v9, v25
	v_max_f32_e32 v6, 0, v6
	v_max_f32_e32 v7, 0, v7
	v_max_f32_e32 v8, 0, v8
	v_cvt_pk_f16_f32 v7, v7, v8
	v_cvt_pk_f16_f32 v6, v6, v10
	v_add_f32_e32 v3, v3, v19
	ds_write_b64 v199, v[6:7] offset:64
	v_add_f32_e32 v2, v2, v18
	v_max_f32_e32 v6, 0, v3
	v_add_f32_e32 v3, v4, v20
	v_add_f32_e32 v4, v5, v21
	v_max_f32_e32 v2, 0, v2
	v_max_f32_e32 v3, 0, v3
	v_max_f32_e32 v4, 0, v4
	v_cvt_pk_f16_f32 v3, v3, v4
	v_cvt_pk_f16_f32 v2, v2, v6
	ds_write_b64 v199, v[2:3] offset:96
	s_waitcnt lgkmcnt(0)
	ds_read_b128 v[208:211], v202
	ds_read_b128 v[212:215], v202 offset:1152
	ds_bpermute_b32 v216, v203, v34
	ds_bpermute_b32 v217, v203, v35
	ds_bpermute_b32 v218, v204, v34
	ds_bpermute_b32 v219, v204, v35
	v_add_u32_e32 v222, 32, v205
	v_cmp_gt_u32_e64 s[38:39], s24, v222
	v_add_u32_e32 v222, 8, v222
	v_cmp_gt_u32_e64 s[40:41], s24, v222
	s_waitcnt lgkmcnt(0)
	v_lshl_add_u64 v[216:217], v[216:217], 0, v[220:221]
	v_lshl_add_u64 v[218:219], v[218:219], 0, v[220:221]
	s_mov_b64 s[42:43], exec
	s_and_b64 exec, s[42:43], s[38:39]
	global_store_dwordx4 v[216:217], v[208:211], off
	s_and_b64 exec, s[42:43], s[40:41]
	global_store_dwordx4 v[218:219], v[212:215], off
	s_mov_b64 exec, s[42:43]

.LBB4_55:
	s_or_b64 exec, exec, s[4:5]
	s_waitcnt vmcnt(1)
	ds_write_b128 v78, v[14:17] offset:40960
	s_waitcnt vmcnt(0)
	ds_write_b128 v78, v[22:25] offset:49152
	s_waitcnt lgkmcnt(0)
	s_barrier
	ds_read_b128 v[14:17], v82 offset:40960
	ds_read_b128 v[18:21], v81 offset:12288
	ds_read_b128 v[22:25], v81 offset:14336
	ds_read_b128 v[46:49], v82 offset:43008
	ds_read_b128 v[50:53], v79 offset:12288
	s_waitcnt lgkmcnt(3)
	v_mfma_f32_16x16x32_f16 v[42:45], v[14:17], v[18:21], v[42:45]
	ds_read_b128 v[54:57], v80 offset:43008
	s_lshl_b64 s[0:1], s[0:1], 1
	s_add_u32 s0, s10, s0
	s_waitcnt lgkmcnt(2)
	v_mfma_f32_16x16x32_f16 v[10:13], v[46:49], v[18:21], v[10:13]
	s_addc_u32 s1, s11, s1
	v_lshlrev_b32_e32 v0, 1, v67
	v_mov_b32_e32 v1, 0
	v_mfma_f32_16x16x32_f16 v[18:21], v[14:17], v[22:25], v[34:37]
	v_cmp_gt_u32_e32 vcc, s24, v63
	v_mfma_f32_16x16x32_f16 v[34:37], v[46:49], v[22:25], v[38:41]
	ds_read_b128 v[22:25], v81 offset:16384
	s_nop 1
	ds_read_b128 v[38:41], v80 offset:40960
	s_waitcnt lgkmcnt(1)
	v_mfma_f32_16x16x32_f16 v[14:17], v[14:17], v[22:25], v[30:33]
	v_mfma_f32_16x16x32_f16 v[46:49], v[46:49], v[22:25], v[26:29]
	s_waitcnt lgkmcnt(0)
	v_mfma_f32_16x16x32_f16 v[30:33], v[38:41], v[50:53], v[42:45]
	v_mfma_f32_16x16x32_f16 v[26:29], v[54:57], v[50:53], v[10:13]
	s_nop 2
	ds_read_b128 v[10:13], v79 offset:14336
	ds_read_b128 v[42:45], v79 offset:16384
	s_waitcnt lgkmcnt(1)
	v_mfma_f32_16x16x32_f16 v[22:25], v[38:41], v[10:13], v[18:21]
	v_mfma_f32_16x16x32_f16 v[18:21], v[54:57], v[10:13], v[34:37]
	v_lshl_add_u64 v[10:11], s[0:1], 0, v[0:1]
	v_lshlrev_b32_e32 v0, 1, v65
	v_lshl_add_u64 v[0:1], v[10:11], 0, v[0:1]
	s_waitcnt lgkmcnt(0)
	v_mfma_f32_16x16x32_f16 v[14:17], v[38:41], v[42:45], v[14:17]
	v_mfma_f32_16x16x32_f16 v[10:13], v[54:57], v[42:45], v[46:49]
	v_mbcnt_lo_u32_b32 v196, -1, 0
	v_mbcnt_hi_u32_b32 v196, -1, v196
	v_and_b32_e32 v197, 15, v196
	v_lshrrev_b32_e32 v198, 4, v196
	v_lshrrev_b32_e32 v222, 10, v78
	s_nop 0
	v_readfirstlane_b32 s36, v222
	s_nop 3
	s_and_b32 s36, s36, 7
	s_mulk_i32 s36, 0x500
	s_add_u32 s36, s36, 0x6000
	v_mul_u32_u24_e32 v199, 0x50, v197
	v_lshl_add_u32 v199, v198, 3, v199
	v_add_u32_e32 v199, s36, v199
	v_lshrrev_b32_e32 v200, 2, v196
	v_and_b32_e32 v201, 3, v196
	v_mul_u32_u24_e32 v202, 0x50, v200
	v_lshl_add_u32 v202, v201, 4, v202
	v_add_u32_e32 v202, s36, v202
	v_lshlrev_b32_e32 v203, 2, v200
	v_add_u32_e32 v204, 32, v203
	v_lshlrev_b32_e32 v220, 4, v201
	v_mov_b32_e32 v221, 0
	v_sub_u32_e32 v205, v63, v197
	v_add_u32_e32 v205, v205, v200
	s_mov_b64 s[0:1], exec
	s_cbranch_execz .LBB4_57
	v_add_f32_e32 v31, v7, v31
	v_ashrrev_i32_e32 v67, 31, v66
	v_add_f32_e32 v30, v6, v30
	v_max_f32_e32 v36, 0, v31
	v_add_f32_e32 v31, v8, v32
	v_add_f32_e32 v32, v9, v33
	v_lshlrev_b64 v[34:35], 11, v[66:67]
	v_max_f32_e32 v30, 0, v30
	v_max_f32_e32 v31, 0, v31
	v_max_f32_e32 v32, 0, v32
	v_lshl_add_u64 v[34:35], v[0:1], 0, v[34:35]
	v_cvt_pk_f16_f32 v31, v31, v32
	v_cvt_pk_f16_f32 v30, v30, v36
	v_add_f32_e32 v27, v3, v27
	ds_write_b64 v199, v[30:31]
	v_add_f32_e32 v26, v2, v26
	v_max_f32_e32 v30, 0, v27
	v_add_f32_e32 v27, v4, v28
	v_add_f32_e32 v28, v5, v29
	v_max_f32_e32 v26, 0, v26
	v_max_f32_e32 v27, 0, v27
	v_max_f32_e32 v28, 0, v28
	v_cvt_pk_f16_f32 v27, v27, v28
	v_cvt_pk_f16_f32 v26, v26, v30
	ds_write_b64 v199, v[26:27] offset:32
	s_waitcnt lgkmcnt(0)
	ds_read_b128 v[208:211], v202
	ds_bpermute_b32 v216, v203, v34
	ds_bpermute_b32 v217, v203, v35
	v_add_u32_e32 v222, 0, v205
	v_cmp_gt_u32_e64 s[38:39], s24, v222
	s_waitcnt lgkmcnt(0)
	v_lshl_add_u64 v[216:217], v[216:217], 0, v[220:221]
	s_mov_b64 s[42:43], exec
	s_and_b64 exec, s[42:43], s[38:39]
	global_store_dwordx4 v[216:217], v[208:211], off
	s_mov_b64 exec, s[42:43]
.LBB4_57:
	s_or_b64 exec, exec, s[0:1]
	v_add_u32_e32 v26, 16, v63
	v_cmp_gt_u32_e32 vcc, s24, v26
	s_mov_b64 s[0:1], exec
	s_cbranch_execz .LBB4_59
	v_add_f32_e32 v23, v7, v23
	v_ashrrev_i32_e32 v65, 31, v64
	v_add_f32_e32 v22, v6, v22
	v_max_f32_e32 v28, 0, v23
	v_add_f32_e32 v23, v8, v24
	v_add_f32_e32 v24, v9, v25
	v_lshlrev_b64 v[26:27], 11, v[64:65]
	v_max_f32_e32 v22, 0, v22
	v_max_f32_e32 v23, 0, v23
	v_max_f32_e32 v24, 0, v24
	v_lshl_add_u64 v[26:27], v[0:1], 0, v[26:27]
	v_cvt_pk_f16_f32 v23, v23, v24
	v_cvt_pk_f16_f32 v22, v22, v28
	v_add_f32_e32 v19, v3, v19
	ds_write_b64 v199, v[22:23]
	v_add_f32_e32 v18, v2, v18
	v_max_f32_e32 v22, 0, v19
	v_add_f32_e32 v19, v4, v20
	v_add_f32_e32 v20, v5, v21
	v_max_f32_e32 v18, 0, v18
	v_max_f32_e32 v19, 0, v19
	v_max_f32_e32 v20, 0, v20
	v_cvt_pk_f16_f32 v19, v19, v20
	v_cvt_pk_f16_f32 v18, v18, v22
	ds_write_b64 v199, v[18:19] offset:32
	s_waitcnt lgkmcnt(0)
	ds_read_b128 v[208:211], v202
	ds_bpermute_b32 v216, v203, v26
	ds_bpermute_b32 v217, v203, v27
	v_add_u32_e32 v222, 16, v205
	v_cmp_gt_u32_e64 s[38:39], s24, v222
	s_waitcnt lgkmcnt(0)
	v_lshl_add_u64 v[216:217], v[216:217], 0, v[220:221]
	s_mov_b64 s[42:43], exec
	s_and_b64 exec, s[42:43], s[38:39]
	global_store_dwordx4 v[216:217], v[208:211], off
	s_mov_b64 exec, s[42:43]
.LBB4_59:
	s_or_b64 exec, exec, s[0:1]
	v_add_u32_e32 v18, 32, v63
	v_cmp_gt_u32_e32 vcc, s24, v18
	s_mov_b64 s[0:1], exec
	s_cbranch_execz .LBB4_61
	v_add_f32_e32 v7, v7, v15
	v_ashrrev_i32_e32 v63, 31, v62
	v_add_f32_e32 v6, v6, v14
	v_max_f32_e32 v14, 0, v7
	v_add_f32_e32 v7, v8, v16
	v_add_f32_e32 v8, v9, v17
	v_lshlrev_b64 v[18:19], 11, v[62:63]
	v_max_f32_e32 v6, 0, v6
	v_max_f32_e32 v7, 0, v7
	v_max_f32_e32 v8, 0, v8
	v_lshl_add_u64 v[0:1], v[0:1], 0, v[18:19]
	v_cvt_pk_f16_f32 v7, v7, v8
	v_cvt_pk_f16_f32 v6, v6, v14
	v_add_f32_e32 v3, v3, v11
	ds_write_b64 v199, v[6:7]
	v_add_f32_e32 v2, v2, v10
	v_max_f32_e32 v6, 0, v3
	v_add_f32_e32 v3, v4, v12
	v_add_f32_e32 v4, v5, v13
	v_max_f32_e32 v2, 0, v2
	v_max_f32_e32 v3, 0, v3
	v_max_f32_e32 v4, 0, v4
	v_cvt_pk_f16_f32 v3, v3, v4
	v_cvt_pk_f16_f32 v2, v2, v6
	ds_write_b64 v199, v[2:3] offset:32
	s_waitcnt lgkmcnt(0)
	ds_read_b128 v[208:211], v202
	ds_bpermute_b32 v216, v203, v0
	ds_bpermute_b32 v217, v203, v1
	v_add_u32_e32 v222, 32, v205
	v_cmp_gt_u32_e64 s[38:39], s24, v222
	s_waitcnt lgkmcnt(0)
	v_lshl_add_u64 v[216:217], v[216:217], 0, v[220:221]
	s_mov_b64 s[42:43], exec
	s_and_b64 exec, s[42:43], s[38:39]
	global_store_dwordx4 v[216:217], v[208:211], off
	s_mov_b64 exec, s[42:43]

	.amdhsa_kernel _Z11gemm_kernelILi0ELi96ELi256ELi128ELi2ELi4ELi2ELi2ELi64EEvPKDF16_PDF16_PKiS4_S1_S1_PKf
		.amdhsa_group_segment_fixed_size 0
		.amdhsa_private_segment_fixed_size 0
		.amdhsa_kernarg_size 56
		.amdhsa_user_sgpr_count 2
		.amdhsa_user_sgpr_dispatch_ptr 0
		.amdhsa_user_sgpr_queue_ptr 0
		.amdhsa_user_sgpr_kernarg_segment_ptr 1
		.amdhsa_user_sgpr_dispatch_id 0
		.amdhsa_user_sgpr_kernarg_preload_length 0
		.amdhsa_user_sgpr_kernarg_preload_offset 0
		.amdhsa_user_sgpr_private_segment_size 0
		.amdhsa_uses_dynamic_stack 0
		.amdhsa_enable_private_segment 0
		.amdhsa_system_sgpr_workgroup_id_x 1
		.amdhsa_system_sgpr_workgroup_id_y 0
		.amdhsa_system_sgpr_workgroup_id_z 0
		.amdhsa_system_sgpr_workgroup_info 0
		.amdhsa_system_vgpr_workitem_id 0
		.amdhsa_next_free_vgpr 224
		.amdhsa_next_free_sgpr 44
		.amdhsa_accum_offset 224
		.amdhsa_reserve_vcc 1
		.amdhsa_float_round_mode_32 0
		.amdhsa_float_round_mode_16_64 0
		.amdhsa_float_denorm_mode_32 3
		.amdhsa_float_denorm_mode_16_64 3
		.amdhsa_dx10_clamp 1
		.amdhsa_ieee_mode 1
		.amdhsa_fp16_overflow 0
		.amdhsa_tg_split 0
		.amdhsa_exception_fp_ieee_invalid_op 0
		.amdhsa_exception_fp_denorm_src 0
		.amdhsa_exception_fp_ieee_div_zero 0
		.amdhsa_exception_fp_ieee_overflow 0
		.amdhsa_exception_fp_ieee_underflow 0
		.amdhsa_exception_fp_ieee_inexact 0
		.amdhsa_exception_int_div_zero 0
	.end_amdhsa_kernel

_Z11gemm_kernelILi1ELi64ELi128ELi128ELi2ELi4ELi2ELi2ELi128EEvPKDF16_PDF16_PKiS4_S1_S1_PKf:
	s_cmp_gt_i32 s2, -1
	s_cbranch_scc0 .LBB7_2
	s_lshr_b32 s3, s2, 3
	s_and_b32 s3, s3, 0xffffff8
	s_and_b32 s4, s2, 7
	s_bfe_u32 s10, s2, 0x30003
	s_or_b32 s4, s3, s4
	s_mov_b64 s[6:7], -1
	s_cbranch_execz .LBB7_3
	s_branch .LBB7_4

amdhsa.kernels:
  - .agpr_count:     0
    .args:
      - .actual_access:  read_only
        .address_space:  global
        .offset:         0
        .size:           8
        .value_kind:     global_buffer
      - .actual_access:  read_only
        .address_space:  global
        .offset:         8
        .size:           8
        .value_kind:     global_buffer
      - .actual_access:  read_only
        .address_space:  global
        .offset:         16
        .size:           8
        .value_kind:     global_buffer
      - .actual_access:  read_only
        .address_space:  global
        .offset:         24
        .size:           8
        .value_kind:     global_buffer
      - .actual_access:  read_only
        .address_space:  global
        .offset:         32
        .size:           8
        .value_kind:     global_buffer
      - .actual_access:  read_only
        .address_space:  global
        .offset:         40
        .size:           8
        .value_kind:     global_buffer
      - .actual_access:  read_only
        .address_space:  global
        .offset:         48
        .size:           8
        .value_kind:     global_buffer
      - .actual_access:  read_only
        .address_space:  global
        .offset:         56
        .size:           8
        .value_kind:     global_buffer
      - .actual_access:  write_only
        .address_space:  global
        .offset:         64
        .size:           8
        .value_kind:     global_buffer
    .group_segment_fixed_size: 16832
    .kernarg_segment_align: 8
    .kernarg_segment_size: 72
    .language:       OpenCL C
    .language_version:
      - 2
      - 0
    .max_flat_workgroup_size: 256
    .name:           _Z12front_kernelPKiS0_S0_PKfS2_S2_S2_S2_Pc
    .private_segment_fixed_size: 0
    .sgpr_count:     106
    .sgpr_spill_count: 398
    .symbol:         _Z12front_kernelPKiS0_S0_PKfS2_S2_S2_S2_Pc.kd
    .uniform_work_group_size: 1
    .uses_dynamic_stack: false
    .vgpr_count:     78
    .vgpr_spill_count: 0
    .wavefront_size: 64
  - .agpr_count:     0
    .args:
      - .actual_access:  read_only
        .address_space:  global
        .offset:         0
        .size:           8
        .value_kind:     global_buffer
      - .actual_access:  read_only
        .address_space:  global
        .offset:         8
        .size:           8
        .value_kind:     global_buffer
      - .actual_access:  read_only
        .address_space:  global
        .offset:         16
        .size:           8
        .value_kind:     global_buffer
      - .actual_access:  write_only
        .address_space:  global
        .offset:         24
        .size:           8
        .value_kind:     global_buffer
    .group_segment_fixed_size: 0
    .kernarg_segment_align: 8
    .kernarg_segment_size: 32
    .language:       OpenCL C
    .language_version:
      - 2
      - 0
    .max_flat_workgroup_size: 256
    .name:           _Z12final_kernelPKDF16_PKfS2_Pf
    .private_segment_fixed_size: 0
    .sgpr_count:     14
    .sgpr_spill_count: 0
    .symbol:         _Z12final_kernelPKDF16_PKfS2_Pf.kd
    .uniform_work_group_size: 1
    .uses_dynamic_stack: false
    .vgpr_count:     40
    .vgpr_spill_count: 0
    .wavefront_size: 64
  - .agpr_count:     0
    .args:
      - .address_space:  global
        .offset:         0
        .size:           8
        .value_kind:     global_buffer
      - .actual_access:  write_only
        .address_space:  global
        .offset:         8
        .size:           8
        .value_kind:     global_buffer
      - .actual_access:  read_only
        .address_space:  global
        .offset:         16
        .size:           8
        .value_kind:     global_buffer
      - .actual_access:  read_only
        .address_space:  global
        .offset:         24
        .size:           8
        .value_kind:     global_buffer
      - .address_space:  global
        .offset:         32
        .size:           8
        .value_kind:     global_buffer
      - .address_space:  global
        .offset:         40
        .size:           8
        .value_kind:     global_buffer
      - .actual_access:  read_only
        .address_space:  global
        .offset:         48
        .size:           8
        .value_kind:     global_buffer
      - .offset:         56
        .size:           4
        .value_kind:     by_value
      - .actual_access:  read_only
        .address_space:  global
        .offset:         64
        .size:           8
        .value_kind:     global_buffer
      - .actual_access:  write_only
        .address_space:  global
        .offset:         72
        .size:           8
        .value_kind:     global_buffer
    .group_segment_fixed_size: 0
    .kernarg_segment_align: 8
    .kernarg_segment_size: 80
    .language:       OpenCL C
    .language_version:
      - 2
      - 0
    .max_flat_workgroup_size: 512
    .name:           _Z16gemm_glds_kernelILi2EEvPKDF16_PDF16_PKiS4_S1_S1_PKfiS6_Pc
    .private_segment_fixed_size: 0
    .sgpr_count:     50
    .sgpr_spill_count: 0
    .symbol:         _Z16gemm_glds_kernelILi2EEvPKDF16_PDF16_PKiS4_S1_S1_PKfiS6_Pc.kd
    .uniform_work_group_size: 1
    .uses_dynamic_stack: false
    .vgpr_count:     186
    .vgpr_spill_count: 0
    .wavefront_size: 64
  - .agpr_count:     0
    .args:
      - .actual_access:  read_only
        .address_space:  global
        .offset:         0
        .size:           8
        .value_kind:     global_buffer
      - .actual_access:  write_only
        .address_space:  global
        .offset:         8
        .size:           8
        .value_kind:     global_buffer
      - .actual_access:  read_only
        .address_space:  global
        .offset:         16
        .size:           8
        .value_kind:     global_buffer
      - .actual_access:  read_only
        .address_space:  global
        .offset:         24
        .size:           8
        .value_kind:     global_buffer
      - .actual_access:  read_only
        .address_space:  global
        .offset:         32
        .size:           8
        .value_kind:     global_buffer
      - .actual_access:  read_only
        .address_space:  global
        .offset:         40
        .size:           8
        .value_kind:     global_buffer
      - .actual_access:  read_only
        .address_space:  global
        .offset:         48
        .size:           8
        .value_kind:     global_buffer
    .group_segment_fixed_size: 0
    .kernarg_segment_align: 8
    .kernarg_segment_size: 56
    .language:       OpenCL C
    .language_version:
      - 2
      - 0
    .max_flat_workgroup_size: 512
    .name:           _Z11gemm_kernelILi0ELi192ELi256ELi128ELi2ELi4ELi2ELi2ELi64EEvPKDF16_PDF16_PKiS4_S1_S1_PKf
    .private_segment_fixed_size: 0
    .sgpr_count:     30
    .sgpr_spill_count: 0
    .symbol:         _Z11gemm_kernelILi0ELi192ELi256ELi128ELi2ELi4ELi2ELi2ELi64EEvPKDF16_PDF16_PKiS4_S1_S1_PKf.kd
    .uniform_work_group_size: 1
    .uses_dynamic_stack: false
    .vgpr_count:     254
    .vgpr_spill_count: 0
    .wavefront_size: 64
  - .agpr_count:     0
    .args:
      - .actual_access:  read_only
        .address_space:  global
        .offset:         0
        .size:           8
        .value_kind:     global_buffer
      - .actual_access:  write_only
        .address_space:  global
        .offset:         8
        .size:           8
        .value_kind:     global_buffer
      - .actual_access:  read_only
        .address_space:  global
        .offset:         16
        .size:           8
        .value_kind:     global_buffer
      - .actual_access:  read_only
        .address_space:  global
        .offset:         24
        .size:           8
        .value_kind:     global_buffer
      - .actual_access:  read_only
        .address_space:  global
        .offset:         32
        .size:           8
        .value_kind:     global_buffer
      - .actual_access:  read_only
        .address_space:  global
        .offset:         40
        .size:           8
        .value_kind:     global_buffer
      - .actual_access:  read_only
        .address_space:  global
        .offset:         48
        .size:           8
        .value_kind:     global_buffer
    .group_segment_fixed_size: 0
    .kernarg_segment_align: 8
    .kernarg_segment_size: 56
    .language:       OpenCL C
    .language_version:
      - 2
      - 0
    .max_flat_workgroup_size: 512
    .name:           _Z11gemm_kernelILi0ELi96ELi256ELi128ELi2ELi4ELi2ELi2ELi64EEvPKDF16_PDF16_PKiS4_S1_S1_PKf
    .private_segment_fixed_size: 0
    .sgpr_count:     32
    .sgpr_spill_count: 0
    .symbol:         _Z11gemm_kernelILi0ELi96ELi256ELi128ELi2ELi4ELi2ELi2ELi64EEvPKDF16_PDF16_PKiS4_S1_S1_PKf.kd
    .uniform_work_group_size: 1
    .uses_dynamic_stack: false
    .vgpr_count:     224
    .vgpr_spill_count: 0
    .wavefront_size: 64
  - .agpr_count:     0
    .args:
      - .address_space:  global
        .offset:         0
        .size:           8
        .value_kind:     global_buffer
      - .actual_access:  write_only
        .address_space:  global
        .offset:         8
        .size:           8
        .value_kind:     global_buffer
      - .actual_access:  read_only
        .address_space:  global
        .offset:         16
        .size:           8
        .value_kind:     global_buffer
      - .actual_access:  read_only
        .address_space:  global
        .offset:         24
        .size:           8
        .value_kind:     global_buffer
      - .address_space:  global
        .offset:         32
        .size:           8
        .value_kind:     global_buffer
      - .address_space:  global
        .offset:         40
        .size:           8
        .value_kind:     global_buffer
      - .actual_access:  read_only
        .address_space:  global
        .offset:         48
        .size:           8
        .value_kind:     global_buffer
    .group_segment_fixed_size: 0
    .kernarg_segment_align: 8
    .kernarg_segment_size: 56
    .language:       OpenCL C
    .language_version:
      - 2
      - 0
    .max_flat_workgroup_size: 256
    .name:           _Z15gemm_dma_kernelILi0ELi96ELi128ELi64ELi2ELi2ELi3EEvPKDF16_PDF16_PKiS4_S1_S1_PKf
    .private_segment_fixed_size: 0
    .sgpr_count:     33
    .sgpr_spill_count: 0
    .symbol:         _Z15gemm_dma_kernelILi0ELi96ELi128ELi64ELi2ELi2ELi3EEvPKDF16_PDF16_PKiS4_S1_S1_PKf.kd
    .uniform_work_group_size: 1
    .uses_dynamic_stack: false
    .vgpr_count:     171
    .vgpr_spill_count: 0
    .wavefront_size: 64
  - .agpr_count:     0
    .args:
      - .actual_access:  read_only
        .address_space:  global
        .offset:         0
        .size:           8
        .value_kind:     global_buffer
      - .actual_access:  write_only
        .address_space:  global
        .offset:         8
        .size:           8
        .value_kind:     global_buffer
      - .actual_access:  read_only
        .address_space:  global
        .offset:         16
        .size:           8
        .value_kind:     global_buffer
      - .actual_access:  read_only
        .address_space:  global
        .offset:         24
        .size:           8
        .value_kind:     global_buffer
      - .actual_access:  read_only
        .address_space:  global
        .offset:         32
        .size:           8
        .value_kind:     global_buffer
      - .actual_access:  read_only
        .address_space:  global
        .offset:         40
        .size:           8
        .value_kind:     global_buffer
      - .actual_access:  read_only
        .address_space:  global
        .offset:         48
        .size:           8
        .value_kind:     global_buffer
    .group_segment_fixed_size: 0
    .kernarg_segment_align: 8
    .kernarg_segment_size: 56
    .language:       OpenCL C
    .language_version:
      - 2
      - 0
    .max_flat_workgroup_size: 256
    .name:           _Z11gemm_kernelILi0ELi48ELi128ELi64ELi1ELi4ELi2ELi2ELi128EEvPKDF16_PDF16_PKiS4_S1_S1_PKf
    .private_segment_fixed_size: 0
    .sgpr_count:     30
    .sgpr_spill_count: 0
    .symbol:         _Z11gemm_kernelILi0ELi48ELi128ELi64ELi1ELi4ELi2ELi2ELi128EEvPKDF16_PDF16_PKiS4_S1_S1_PKf.kd
    .uniform_work_group_size: 1
    .uses_dynamic_stack: false
    .vgpr_count:     208
    .vgpr_spill_count: 0
    .wavefront_size: 64
  - .agpr_count:     0
    .args:
      - .actual_access:  read_only
        .address_space:  global
        .offset:         0
        .size:           8
        .value_kind:     global_buffer
      - .actual_access:  write_only
        .address_space:  global
        .offset:         8
        .size:           8
        .value_kind:     global_buffer
      - .actual_access:  read_only
        .address_space:  global
        .offset:         16
        .size:           8
        .value_kind:     global_buffer
      - .actual_access:  read_only
        .address_space:  global
        .offset:         24
        .size:           8
        .value_kind:     global_buffer
      - .actual_access:  read_only
        .address_space:  global
        .offset:         32
        .size:           8
        .value_kind:     global_buffer
      - .actual_access:  read_only
        .address_space:  global
        .offset:         40
        .size:           8
        .value_kind:     global_buffer
      - .actual_access:  read_only
        .address_space:  global
        .offset:         48
        .size:           8
        .value_kind:     global_buffer
    .group_segment_fixed_size: 0
    .kernarg_segment_align: 8
    .kernarg_segment_size: 56
    .language:       OpenCL C
    .language_version:
      - 2
      - 0
    .max_flat_workgroup_size: 512
    .name:           _Z11gemm_kernelILi1ELi64ELi128ELi128ELi2ELi4ELi2ELi2ELi128EEvPKDF16_PDF16_PKiS4_S1_S1_PKf
    .private_segment_fixed_size: 0
    .sgpr_count:     23
    .sgpr_spill_count: 0
    .symbol:         _Z11gemm_kernelILi1ELi64ELi128ELi128ELi2ELi4ELi2ELi2ELi128EEvPKDF16_PDF16_PKiS4_S1_S1_PKf.kd
    .uniform_work_group_size: 1
    .uses_dynamic_stack: false
    .vgpr_count:     117
    .vgpr_spill_count: 0
    .wavefront_size: 64
